# back-edge rotation: K-loop counter/pointer updates and compare moved from behind the last barrier into the last MFMA block (all 10 loops)
# baseline (speedup 1.0000x reference)
.LBB0_261:
	ds_read_b128 v[144:147], v170
	ds_read_b128 v[148:151], v170 offset:1024
	ds_read_b128 v[174:177], v170 offset:2048
	ds_read_b128 v[178:181], v170 offset:3072
	ds_read_b128 v[182:185], v171
	ds_read_b128 v[186:189], v171 offset:1024
	ds_read_b128 v[190:193], v171 offset:2048
	ds_read_b128 v[194:197], v171 offset:3072
	s_add_u32 s26, s80, 0xfff80080
	s_addc_u32 s27, s81, -1
	s_cmp_eq_u32 vcc_hi, 28
	s_cselect_b32 s83, s69, s27
	s_cselect_b32 s82, s75, s26
	s_cselect_b32 s27, s57, vcc_lo
	s_cselect_b32 s26, s96, s97
	v_lshl_add_u64 v[152:153], s[80:81], 0, v[134:135]
	s_add_i32 m0, s87, 0xc000
	ds_read_b128 v[198:201], v172
	ds_read_b128 v[202:205], v172 offset:1024
	ds_read_b128 v[206:209], v172 offset:2048
	ds_read_b128 v[210:213], v172 offset:3072
	ds_read_b128 v[214:217], v172 offset:4096
	ds_read_b128 v[220:223], v172 offset:5120
	ds_read_b128 v[224:227], v172 offset:6144
	ds_read_b128 v[228:231], v172 offset:7168
	global_load_lds_dwordx4 v[152:153], off
	v_lshl_add_u64 v[152:153], s[80:81], 0, v[138:139]
	s_add_i32 m0, s87, 0xe000
	s_nop 0
	global_load_lds_dwordx4 v[152:153], off
	s_waitcnt vmcnt(8)
	s_waitcnt lgkmcnt(0)
	s_barrier
	v_mfma_f32_16x16x32_bf16 v[122:125], v[144:147], v[198:201], v[122:125]
	v_mfma_f32_16x16x32_bf16 v[118:121], v[174:177], v[198:201], v[118:121]
	v_mfma_f32_16x16x32_bf16 v[106:109], v[144:147], v[206:209], v[106:109]
	v_mfma_f32_16x16x32_bf16 v[102:105], v[174:177], v[206:209], v[102:105]
	v_mfma_f32_16x16x32_bf16 v[90:93], v[144:147], v[214:217], v[90:93]
	v_mfma_f32_16x16x32_bf16 v[86:89], v[174:177], v[214:217], v[86:89]
	v_mfma_f32_16x16x32_bf16 v[74:77], v[144:147], v[224:227], v[74:77]
	v_mfma_f32_16x16x32_bf16 v[70:73], v[174:177], v[224:227], v[70:73]
	v_mfma_f32_16x16x32_bf16 v[122:125], v[148:151], v[202:205], v[122:125]
	v_mfma_f32_16x16x32_bf16 v[118:121], v[178:181], v[202:205], v[118:121]
	v_mfma_f32_16x16x32_bf16 v[106:109], v[148:151], v[210:213], v[106:109]
	v_mfma_f32_16x16x32_bf16 v[102:105], v[178:181], v[210:213], v[102:105]
	v_mfma_f32_16x16x32_bf16 v[90:93], v[148:151], v[220:223], v[90:93]
	v_mfma_f32_16x16x32_bf16 v[86:89], v[178:181], v[220:223], v[86:89]
	v_mfma_f32_16x16x32_bf16 v[74:77], v[148:151], v[228:231], v[74:77]
	v_mfma_f32_16x16x32_bf16 v[70:73], v[178:181], v[228:231], v[70:73]
	v_mfma_f32_16x16x32_bf16 v[126:129], v[182:185], v[198:201], v[126:129]
	v_mfma_f32_16x16x32_bf16 v[114:117], v[190:193], v[198:201], v[114:117]
	v_mfma_f32_16x16x32_bf16 v[110:113], v[182:185], v[206:209], v[110:113]
	v_mfma_f32_16x16x32_bf16 v[98:101], v[190:193], v[206:209], v[98:101]
	v_mfma_f32_16x16x32_bf16 v[94:97], v[182:185], v[214:217], v[94:97]
	v_mfma_f32_16x16x32_bf16 v[82:85], v[190:193], v[214:217], v[82:85]
	v_mfma_f32_16x16x32_bf16 v[78:81], v[182:185], v[224:227], v[78:81]
	v_mfma_f32_16x16x32_bf16 v[66:69], v[190:193], v[224:227], v[66:69]
	v_mfma_f32_16x16x32_bf16 v[126:129], v[186:189], v[202:205], v[126:129]
	v_mfma_f32_16x16x32_bf16 v[114:117], v[194:197], v[202:205], v[114:117]
	v_mfma_f32_16x16x32_bf16 v[110:113], v[186:189], v[210:213], v[110:113]
	v_mfma_f32_16x16x32_bf16 v[98:101], v[194:197], v[210:213], v[98:101]
	v_mfma_f32_16x16x32_bf16 v[94:97], v[186:189], v[220:223], v[94:97]
	v_mfma_f32_16x16x32_bf16 v[82:85], v[194:197], v[220:223], v[82:85]
	v_mfma_f32_16x16x32_bf16 v[78:81], v[186:189], v[228:231], v[78:81]
	v_mfma_f32_16x16x32_bf16 v[66:69], v[194:197], v[228:231], v[66:69]
	s_barrier
	v_lshl_add_u64 v[152:153], s[26:27], 0, v[162:163]
	s_add_i32 s26, s94, s86
	s_mov_b32 m0, s26
	ds_read_b128 v[198:201], v172 offset:16384
	ds_read_b128 v[202:205], v172 offset:17408
	ds_read_b128 v[206:209], v172 offset:18432
	ds_read_b128 v[210:213], v172 offset:19456
	ds_read_b128 v[214:217], v172 offset:20480
	ds_read_b128 v[220:223], v172 offset:21504
	ds_read_b128 v[224:227], v172 offset:22528
	ds_read_b128 v[228:231], v172 offset:23552
	global_load_lds_dwordx4 v[152:153], off
	v_lshl_add_u64 v[232:233], v[152:153], 0, s[10:11]
	s_add_i32 m0, s26, 0x2000
	s_add_i32 s26, s95, s86
	global_load_lds_dwordx4 v[232:233], off
	v_lshl_add_u64 v[232:233], v[152:153], 0, s[12:13]
	s_mov_b32 m0, s26
	v_lshl_add_u64 v[234:235], s[82:83], 0, v[132:133]
	global_load_lds_dwordx4 v[232:233], off
	v_lshl_add_u64 v[232:233], v[152:153], 0, s[14:15]
	s_add_i32 m0, s26, 0x2000
	s_nop 0
	global_load_lds_dwordx4 v[232:233], off
	v_lshl_add_u64 v[232:233], s[82:83], 0, v[130:131]
	s_mov_b32 m0, s87
	s_nop 0
	global_load_lds_dwordx4 v[232:233], off
	s_mov_b32 m0, s88
	s_nop 0
	global_load_lds_dwordx4 v[234:235], off
	s_waitcnt vmcnt(8)
	s_waitcnt lgkmcnt(0)
	s_barrier
	v_mfma_f32_16x16x32_bf16 v[58:61], v[144:147], v[198:201], v[58:61]
	v_mfma_f32_16x16x32_bf16 v[54:57], v[174:177], v[198:201], v[54:57]
	v_mfma_f32_16x16x32_bf16 v[42:45], v[144:147], v[206:209], v[42:45]
	v_mfma_f32_16x16x32_bf16 v[38:41], v[174:177], v[206:209], v[38:41]
	v_mfma_f32_16x16x32_bf16 v[26:29], v[144:147], v[214:217], v[26:29]
	v_mfma_f32_16x16x32_bf16 v[22:25], v[174:177], v[214:217], v[22:25]
	v_mfma_f32_16x16x32_bf16 v[10:13], v[144:147], v[224:227], v[10:13]
	v_mfma_f32_16x16x32_bf16 v[6:9], v[174:177], v[224:227], v[6:9]
	v_mfma_f32_16x16x32_bf16 v[58:61], v[148:151], v[202:205], v[58:61]
	v_mfma_f32_16x16x32_bf16 v[54:57], v[178:181], v[202:205], v[54:57]
	v_mfma_f32_16x16x32_bf16 v[42:45], v[148:151], v[210:213], v[42:45]
	v_mfma_f32_16x16x32_bf16 v[38:41], v[178:181], v[210:213], v[38:41]
	v_mfma_f32_16x16x32_bf16 v[26:29], v[148:151], v[220:223], v[26:29]
	v_mfma_f32_16x16x32_bf16 v[22:25], v[178:181], v[220:223], v[22:25]
	v_mfma_f32_16x16x32_bf16 v[10:13], v[148:151], v[228:231], v[10:13]
	v_mfma_f32_16x16x32_bf16 v[6:9], v[178:181], v[228:231], v[6:9]
	v_mfma_f32_16x16x32_bf16 v[62:65], v[182:185], v[198:201], v[62:65]
	v_mfma_f32_16x16x32_bf16 v[50:53], v[190:193], v[198:201], v[50:53]
	v_mfma_f32_16x16x32_bf16 v[46:49], v[182:185], v[206:209], v[46:49]
	v_mfma_f32_16x16x32_bf16 v[34:37], v[190:193], v[206:209], v[34:37]
	v_mfma_f32_16x16x32_bf16 v[30:33], v[182:185], v[214:217], v[30:33]
	v_mfma_f32_16x16x32_bf16 v[18:21], v[190:193], v[214:217], v[18:21]
	v_mfma_f32_16x16x32_bf16 v[14:17], v[182:185], v[224:227], v[14:17]
	v_mfma_f32_16x16x32_bf16 v[2:5], v[190:193], v[224:227], v[2:5]
	v_mfma_f32_16x16x32_bf16 v[62:65], v[186:189], v[202:205], v[62:65]
	v_mfma_f32_16x16x32_bf16 v[50:53], v[194:197], v[202:205], v[50:53]
	v_mfma_f32_16x16x32_bf16 v[46:49], v[186:189], v[210:213], v[46:49]
	v_mfma_f32_16x16x32_bf16 v[34:37], v[194:197], v[210:213], v[34:37]
	v_mfma_f32_16x16x32_bf16 v[30:33], v[186:189], v[220:223], v[30:33]
	v_mfma_f32_16x16x32_bf16 v[18:21], v[194:197], v[220:223], v[18:21]
	v_mfma_f32_16x16x32_bf16 v[14:17], v[186:189], v[228:231], v[14:17]
	v_mfma_f32_16x16x32_bf16 v[2:5], v[194:197], v[228:231], v[2:5]
	s_barrier
	s_add_i32 s33, 0, 0x18000
	v_add_u32_e32 v136, s33, v167
	s_add_i32 s8, 0, 0x1c000
	ds_read_b128 v[144:147], v136
	ds_read_b128 v[148:151], v136 offset:1024
	ds_read_b128 v[174:177], v136 offset:2048
	ds_read_b128 v[178:181], v136 offset:3072
	v_add_u32_e32 v136, s8, v167
	ds_read_b128 v[182:185], v136
	ds_read_b128 v[186:189], v136 offset:1024
	ds_read_b128 v[190:193], v136 offset:2048
	ds_read_b128 v[194:197], v136 offset:3072
	s_add_u32 s26, s82, 0x80000
	s_addc_u32 s27, s83, 0
	s_mov_b32 m0, s89
	v_lshl_add_u64 v[236:237], s[26:27], 0, v[130:131]
	ds_read_b128 v[198:201], v172 offset:32768
	ds_read_b128 v[202:205], v172 offset:33792
	ds_read_b128 v[206:209], v172 offset:34816
	ds_read_b128 v[210:213], v172 offset:35840
	ds_read_b128 v[214:217], v172 offset:36864
	ds_read_b128 v[220:223], v172 offset:37888
	ds_read_b128 v[224:227], v172 offset:38912
	ds_read_b128 v[228:231], v172 offset:39936
	global_load_lds_dwordx4 v[236:237], off
	v_lshl_add_u64 v[236:237], s[26:27], 0, v[132:133]
	s_mov_b32 m0, s90
	s_nop 0
	global_load_lds_dwordx4 v[236:237], off
	s_waitcnt vmcnt(8)
	s_waitcnt lgkmcnt(0)
	s_barrier
	v_mfma_f32_16x16x32_bf16 v[122:125], v[144:147], v[198:201], v[122:125]
	v_mfma_f32_16x16x32_bf16 v[118:121], v[174:177], v[198:201], v[118:121]
	v_mfma_f32_16x16x32_bf16 v[106:109], v[144:147], v[206:209], v[106:109]
	v_mfma_f32_16x16x32_bf16 v[102:105], v[174:177], v[206:209], v[102:105]
	v_mfma_f32_16x16x32_bf16 v[90:93], v[144:147], v[214:217], v[90:93]
	v_mfma_f32_16x16x32_bf16 v[86:89], v[174:177], v[214:217], v[86:89]
	v_mfma_f32_16x16x32_bf16 v[74:77], v[144:147], v[224:227], v[74:77]
	v_mfma_f32_16x16x32_bf16 v[70:73], v[174:177], v[224:227], v[70:73]
	v_mfma_f32_16x16x32_bf16 v[122:125], v[148:151], v[202:205], v[122:125]
	v_mfma_f32_16x16x32_bf16 v[118:121], v[178:181], v[202:205], v[118:121]
	v_mfma_f32_16x16x32_bf16 v[106:109], v[148:151], v[210:213], v[106:109]
	v_mfma_f32_16x16x32_bf16 v[102:105], v[178:181], v[210:213], v[102:105]
	v_mfma_f32_16x16x32_bf16 v[90:93], v[148:151], v[220:223], v[90:93]
	v_mfma_f32_16x16x32_bf16 v[86:89], v[178:181], v[220:223], v[86:89]
	v_mfma_f32_16x16x32_bf16 v[74:77], v[148:151], v[228:231], v[74:77]
	v_mfma_f32_16x16x32_bf16 v[70:73], v[178:181], v[228:231], v[70:73]
	v_mfma_f32_16x16x32_bf16 v[126:129], v[182:185], v[198:201], v[126:129]
	v_mfma_f32_16x16x32_bf16 v[114:117], v[190:193], v[198:201], v[114:117]
	v_mfma_f32_16x16x32_bf16 v[110:113], v[182:185], v[206:209], v[110:113]
	v_mfma_f32_16x16x32_bf16 v[98:101], v[190:193], v[206:209], v[98:101]
	v_mfma_f32_16x16x32_bf16 v[94:97], v[182:185], v[214:217], v[94:97]
	v_mfma_f32_16x16x32_bf16 v[82:85], v[190:193], v[214:217], v[82:85]
	v_mfma_f32_16x16x32_bf16 v[78:81], v[182:185], v[224:227], v[78:81]
	v_mfma_f32_16x16x32_bf16 v[66:69], v[190:193], v[224:227], v[66:69]
	v_mfma_f32_16x16x32_bf16 v[126:129], v[186:189], v[202:205], v[126:129]
	v_mfma_f32_16x16x32_bf16 v[114:117], v[194:197], v[202:205], v[114:117]
	v_mfma_f32_16x16x32_bf16 v[110:113], v[186:189], v[210:213], v[110:113]
	v_mfma_f32_16x16x32_bf16 v[98:101], v[194:197], v[210:213], v[98:101]
	v_mfma_f32_16x16x32_bf16 v[94:97], v[186:189], v[220:223], v[94:97]
	v_mfma_f32_16x16x32_bf16 v[82:85], v[194:197], v[220:223], v[82:85]
	v_mfma_f32_16x16x32_bf16 v[78:81], v[186:189], v[228:231], v[78:81]
	v_mfma_f32_16x16x32_bf16 v[66:69], v[194:197], v[228:231], v[66:69]
	s_barrier
	s_add_i32 s9, s33, s86
	v_lshl_add_u64 v[236:237], v[152:153], 0, s[20:21]
	s_mov_b32 m0, s9
	ds_read_b128 v[198:201], v172 offset:49152
	ds_read_b128 v[202:205], v172 offset:50176
	ds_read_b128 v[206:209], v172 offset:51200
	ds_read_b128 v[210:213], v172 offset:52224
	ds_read_b128 v[214:217], v172 offset:53248
	ds_read_b128 v[220:223], v172 offset:54272
	ds_read_b128 v[224:227], v172 offset:55296
	ds_read_b128 v[228:231], v172 offset:56320
	global_load_lds_dwordx4 v[236:237], off
	v_lshl_add_u64 v[236:237], v[152:153], 0, s[22:23]
	s_add_i32 m0, s9, 0x2000
	s_add_i32 s8, s8, s86
	global_load_lds_dwordx4 v[236:237], off
	v_lshl_add_u64 v[236:237], v[152:153], 0, s[40:41]
	s_mov_b32 m0, s8
	v_lshl_add_u64 v[152:153], v[152:153], 0, s[44:45]
	global_load_lds_dwordx4 v[236:237], off
	s_add_i32 m0, s8, 0x2000
	s_nop 0
	global_load_lds_dwordx4 v[152:153], off
	v_lshl_add_u64 v[152:153], v[232:233], 0, s[24:25]
	s_mov_b32 m0, s91
	s_nop 0
	global_load_lds_dwordx4 v[152:153], off
	v_lshl_add_u64 v[152:153], v[234:235], 0, s[24:25]
	s_mov_b32 m0, s92
	s_nop 0
	global_load_lds_dwordx4 v[152:153], off
	s_waitcnt vmcnt(8)
	s_waitcnt lgkmcnt(0)
	s_barrier
	v_mfma_f32_16x16x32_bf16 v[58:61], v[144:147], v[198:201], v[58:61]
	s_add_i32 vcc_hi, vcc_hi, 2
	s_add_u32 s97, s97, 0x10000
	s_addc_u32 vcc_lo, vcc_lo, 0
	s_add_u32 s80, s80, 0x100
	s_addc_u32 s81, s81, 0
	s_cmp_gt_u32 vcc_hi, 29
	v_mfma_f32_16x16x32_bf16 v[54:57], v[174:177], v[198:201], v[54:57]
	v_mfma_f32_16x16x32_bf16 v[42:45], v[144:147], v[206:209], v[42:45]
	v_mfma_f32_16x16x32_bf16 v[38:41], v[174:177], v[206:209], v[38:41]
	v_mfma_f32_16x16x32_bf16 v[26:29], v[144:147], v[214:217], v[26:29]
	v_mfma_f32_16x16x32_bf16 v[22:25], v[174:177], v[214:217], v[22:25]
	v_mfma_f32_16x16x32_bf16 v[10:13], v[144:147], v[224:227], v[10:13]
	v_mfma_f32_16x16x32_bf16 v[6:9], v[174:177], v[224:227], v[6:9]
	v_mfma_f32_16x16x32_bf16 v[58:61], v[148:151], v[202:205], v[58:61]
	v_mfma_f32_16x16x32_bf16 v[54:57], v[178:181], v[202:205], v[54:57]
	v_mfma_f32_16x16x32_bf16 v[42:45], v[148:151], v[210:213], v[42:45]
	v_mfma_f32_16x16x32_bf16 v[38:41], v[178:181], v[210:213], v[38:41]
	v_mfma_f32_16x16x32_bf16 v[26:29], v[148:151], v[220:223], v[26:29]
	v_mfma_f32_16x16x32_bf16 v[22:25], v[178:181], v[220:223], v[22:25]
	v_mfma_f32_16x16x32_bf16 v[10:13], v[148:151], v[228:231], v[10:13]
	v_mfma_f32_16x16x32_bf16 v[6:9], v[178:181], v[228:231], v[6:9]
	v_mfma_f32_16x16x32_bf16 v[62:65], v[182:185], v[198:201], v[62:65]
	v_mfma_f32_16x16x32_bf16 v[50:53], v[190:193], v[198:201], v[50:53]
	v_mfma_f32_16x16x32_bf16 v[46:49], v[182:185], v[206:209], v[46:49]
	v_mfma_f32_16x16x32_bf16 v[34:37], v[190:193], v[206:209], v[34:37]
	v_mfma_f32_16x16x32_bf16 v[30:33], v[182:185], v[214:217], v[30:33]
	v_mfma_f32_16x16x32_bf16 v[18:21], v[190:193], v[214:217], v[18:21]
	v_mfma_f32_16x16x32_bf16 v[14:17], v[182:185], v[224:227], v[14:17]
	v_mfma_f32_16x16x32_bf16 v[2:5], v[190:193], v[224:227], v[2:5]
	v_mfma_f32_16x16x32_bf16 v[62:65], v[186:189], v[202:205], v[62:65]
	v_mfma_f32_16x16x32_bf16 v[50:53], v[194:197], v[202:205], v[50:53]
	v_mfma_f32_16x16x32_bf16 v[46:49], v[186:189], v[210:213], v[46:49]
	v_mfma_f32_16x16x32_bf16 v[34:37], v[194:197], v[210:213], v[34:37]
	v_mfma_f32_16x16x32_bf16 v[30:33], v[186:189], v[220:223], v[30:33]
	v_mfma_f32_16x16x32_bf16 v[18:21], v[194:197], v[220:223], v[18:21]
	v_mfma_f32_16x16x32_bf16 v[14:17], v[186:189], v[228:231], v[14:17]
	v_mfma_f32_16x16x32_bf16 v[2:5], v[194:197], v[228:231], v[2:5]
	s_barrier
	s_cbranch_scc0 .LBB0_261
	s_and_b64 vcc, exec, s[50:51]
	s_cbranch_vccz .LBB0_264
	s_barrier

.LBB0_285:
	ds_read_b128 v[26:29], v1
	ds_read_b128 v[30:33], v1 offset:1024
	ds_read_b128 v[18:21], v1 offset:2048
	ds_read_b128 v[22:25], v1 offset:3072
	ds_read_b128 v[10:13], v185
	ds_read_b128 v[14:17], v185 offset:1024
	ds_read_b128 v[2:5], v185 offset:2048
	ds_read_b128 v[6:9], v185 offset:3072
	s_add_u32 s26, s70, 0xfffc0080
	s_addc_u32 s27, s71, -1
	s_cmp_eq_u32 s94, 12
	s_cselect_b32 s73, s51, s27
	s_cselect_b32 s72, s90, s26
	s_cselect_b32 s75, s45, s93
	s_cselect_b32 s74, s91, s92
	v_lshl_add_u64 v[176:177], s[70:71], 0, v[168:169]
	s_add_i32 m0, s33, 0xc000
	ds_read_b128 v[190:193], v186
	ds_read_b128 v[194:197], v186 offset:1024
	ds_read_b128 v[198:201], v186 offset:2048
	ds_read_b128 v[202:205], v186 offset:3072
	ds_read_b128 v[206:209], v186 offset:4096
	ds_read_b128 v[210:213], v186 offset:5120
	ds_read_b128 v[220:223], v186 offset:6144
	ds_read_b128 v[224:227], v186 offset:7168
	global_load_lds_dwordx4 v[176:177], off
	v_lshl_add_u64 v[176:177], s[70:71], 0, v[170:171]
	s_add_i32 m0, s33, 0xe000
	s_nop 0
	global_load_lds_dwordx4 v[176:177], off
	s_waitcnt vmcnt(8)
	s_waitcnt lgkmcnt(0)
	s_barrier
	v_mfma_scale_f32_16x16x128_f8f6f4 v[158:161], v[26:33], v[190:197], v[158:161], v187, v188 op_sel_hi:[0,0,0]
	v_mfma_scale_f32_16x16x128_f8f6f4 v[154:157], v[18:25], v[190:197], v[154:157], v187, v188 op_sel_hi:[0,0,0]
	v_mfma_scale_f32_16x16x128_f8f6f4 v[150:153], v[26:33], v[198:205], v[150:153], v187, v188 op_sel_hi:[0,0,0]
	v_mfma_scale_f32_16x16x128_f8f6f4 v[142:145], v[18:25], v[198:205], v[142:145], v187, v188 op_sel_hi:[0,0,0]
	v_mfma_scale_f32_16x16x128_f8f6f4 v[134:137], v[26:33], v[206:213], v[134:137], v187, v188 op_sel_hi:[0,0,0]
	v_mfma_scale_f32_16x16x128_f8f6f4 v[126:129], v[18:25], v[206:213], v[126:129], v187, v188 op_sel_hi:[0,0,0]
	v_mfma_scale_f32_16x16x128_f8f6f4 v[118:121], v[26:33], v[220:227], v[118:121], v187, v188 op_sel_hi:[0,0,0]
	v_mfma_scale_f32_16x16x128_f8f6f4 v[110:113], v[18:25], v[220:227], v[110:113], v187, v188 op_sel_hi:[0,0,0]
	v_mfma_scale_f32_16x16x128_f8f6f4 v[146:149], v[10:17], v[190:197], v[146:149], v187, v188 op_sel_hi:[0,0,0]
	v_mfma_scale_f32_16x16x128_f8f6f4 v[138:141], v[2:9], v[190:197], v[138:141], v187, v188 op_sel_hi:[0,0,0]
	v_mfma_scale_f32_16x16x128_f8f6f4 v[130:133], v[10:17], v[198:205], v[130:133], v187, v188 op_sel_hi:[0,0,0]
	v_mfma_scale_f32_16x16x128_f8f6f4 v[122:125], v[2:9], v[198:205], v[122:125], v187, v188 op_sel_hi:[0,0,0]
	v_mfma_scale_f32_16x16x128_f8f6f4 v[114:117], v[10:17], v[206:213], v[114:117], v187, v188 op_sel_hi:[0,0,0]
	v_mfma_scale_f32_16x16x128_f8f6f4 v[106:109], v[2:9], v[206:213], v[106:109], v187, v188 op_sel_hi:[0,0,0]
	v_mfma_scale_f32_16x16x128_f8f6f4 v[102:105], v[10:17], v[220:227], v[102:105], v187, v188 op_sel_hi:[0,0,0]
	v_mfma_scale_f32_16x16x128_f8f6f4 v[98:101], v[2:9], v[220:227], v[98:101], v187, v188 op_sel_hi:[0,0,0]
	s_barrier
	s_add_i32 s26, s88, s80
	v_lshl_add_u64 v[176:177], s[74:75], 0, v[162:163]
	s_mov_b32 m0, s26
	ds_read_b128 v[190:193], v186 offset:16384
	ds_read_b128 v[194:197], v186 offset:17408
	ds_read_b128 v[198:201], v186 offset:18432
	ds_read_b128 v[202:205], v186 offset:19456
	ds_read_b128 v[206:209], v186 offset:20480
	ds_read_b128 v[210:213], v186 offset:21504
	ds_read_b128 v[220:223], v186 offset:22528
	ds_read_b128 v[224:227], v186 offset:23552
	global_load_lds_dwordx4 v[176:177], off
	v_lshl_add_u64 v[178:179], v[176:177], 0, s[8:9]
	s_add_i32 m0, s26, 0x2000
	s_add_i32 s26, s89, s80
	global_load_lds_dwordx4 v[178:179], off
	v_lshl_add_u64 v[178:179], v[176:177], 0, s[10:11]
	s_mov_b32 m0, s26
	v_lshl_add_u64 v[180:181], s[72:73], 0, v[166:167]
	global_load_lds_dwordx4 v[178:179], off
	v_lshl_add_u64 v[178:179], v[176:177], 0, s[12:13]
	s_add_i32 m0, s26, 0x2000
	s_nop 0
	global_load_lds_dwordx4 v[178:179], off
	v_lshl_add_u64 v[178:179], s[72:73], 0, v[164:165]
	s_mov_b32 m0, s33
	s_nop 0
	global_load_lds_dwordx4 v[178:179], off
	s_mov_b32 m0, s69
	s_nop 0
	global_load_lds_dwordx4 v[180:181], off
	s_waitcnt vmcnt(8)
	s_waitcnt lgkmcnt(0)
	s_barrier
	v_mfma_scale_f32_16x16x128_f8f6f4 v[94:97], v[26:33], v[190:197], v[94:97], v187, v188 op_sel_hi:[0,0,0]
	v_mfma_scale_f32_16x16x128_f8f6f4 v[90:93], v[18:25], v[190:197], v[90:93], v187, v188 op_sel_hi:[0,0,0]
	v_mfma_scale_f32_16x16x128_f8f6f4 v[86:89], v[26:33], v[198:205], v[86:89], v187, v188 op_sel_hi:[0,0,0]
	v_mfma_scale_f32_16x16x128_f8f6f4 v[78:81], v[18:25], v[198:205], v[78:81], v187, v188 op_sel_hi:[0,0,0]
	v_mfma_scale_f32_16x16x128_f8f6f4 v[70:73], v[26:33], v[206:213], v[70:73], v187, v188 op_sel_hi:[0,0,0]
	v_mfma_scale_f32_16x16x128_f8f6f4 v[62:65], v[18:25], v[206:213], v[62:65], v187, v188 op_sel_hi:[0,0,0]
	v_mfma_scale_f32_16x16x128_f8f6f4 v[54:57], v[26:33], v[220:227], v[54:57], v187, v188 op_sel_hi:[0,0,0]
	v_mfma_scale_f32_16x16x128_f8f6f4 v[46:49], v[18:25], v[220:227], v[46:49], v187, v188 op_sel_hi:[0,0,0]
	v_mfma_scale_f32_16x16x128_f8f6f4 v[82:85], v[10:17], v[190:197], v[82:85], v187, v188 op_sel_hi:[0,0,0]
	v_mfma_scale_f32_16x16x128_f8f6f4 v[74:77], v[2:9], v[190:197], v[74:77], v187, v188 op_sel_hi:[0,0,0]
	v_mfma_scale_f32_16x16x128_f8f6f4 v[66:69], v[10:17], v[198:205], v[66:69], v187, v188 op_sel_hi:[0,0,0]
	v_mfma_scale_f32_16x16x128_f8f6f4 v[58:61], v[2:9], v[198:205], v[58:61], v187, v188 op_sel_hi:[0,0,0]
	v_mfma_scale_f32_16x16x128_f8f6f4 v[50:53], v[10:17], v[206:213], v[50:53], v187, v188 op_sel_hi:[0,0,0]
	v_mfma_scale_f32_16x16x128_f8f6f4 v[42:45], v[2:9], v[206:213], v[42:45], v187, v188 op_sel_hi:[0,0,0]
	v_mfma_scale_f32_16x16x128_f8f6f4 v[38:41], v[10:17], v[220:227], v[38:41], v187, v188 op_sel_hi:[0,0,0]
	v_mfma_scale_f32_16x16x128_f8f6f4 v[34:37], v[2:9], v[220:227], v[34:37], v187, v188 op_sel_hi:[0,0,0]
	s_barrier
	s_add_i32 s74, 0, 0x18000
	s_add_i32 s75, 0, 0x1c000
	v_add_u32_e32 v14, s74, v183
	v_add_u32_e32 v30, s75, v183
	ds_read_b128 v[2:5], v14
	ds_read_b128 v[6:9], v14 offset:1024
	ds_read_b128 v[10:13], v14 offset:2048
	ds_read_b128 v[14:17], v14 offset:3072
	ds_read_b128 v[18:21], v30
	ds_read_b128 v[22:25], v30 offset:1024
	ds_read_b128 v[26:29], v30 offset:2048
	ds_read_b128 v[30:33], v30 offset:3072
	s_add_u32 s26, s72, 0x40000
	s_addc_u32 s27, s73, 0
	s_mov_b32 m0, s83
	v_lshl_add_u64 v[214:215], s[26:27], 0, v[164:165]
	ds_read_b128 v[190:193], v186 offset:32768
	ds_read_b128 v[194:197], v186 offset:33792
	ds_read_b128 v[198:201], v186 offset:34816
	ds_read_b128 v[202:205], v186 offset:35840
	ds_read_b128 v[206:209], v186 offset:36864
	ds_read_b128 v[210:213], v186 offset:37888
	ds_read_b128 v[220:223], v186 offset:38912
	ds_read_b128 v[224:227], v186 offset:39936
	global_load_lds_dwordx4 v[214:215], off
	v_lshl_add_u64 v[214:215], s[26:27], 0, v[166:167]
	s_mov_b32 m0, s84
	s_nop 0
	global_load_lds_dwordx4 v[214:215], off
	s_waitcnt vmcnt(8)
	s_waitcnt lgkmcnt(0)
	s_barrier
	v_mfma_scale_f32_16x16x128_f8f6f4 v[158:161], v[2:9], v[190:197], v[158:161], v187, v188 op_sel_hi:[0,0,0]
	v_mfma_scale_f32_16x16x128_f8f6f4 v[154:157], v[10:17], v[190:197], v[154:157], v187, v188 op_sel_hi:[0,0,0]
	v_mfma_scale_f32_16x16x128_f8f6f4 v[150:153], v[2:9], v[198:205], v[150:153], v187, v188 op_sel_hi:[0,0,0]
	v_mfma_scale_f32_16x16x128_f8f6f4 v[142:145], v[10:17], v[198:205], v[142:145], v187, v188 op_sel_hi:[0,0,0]
	v_mfma_scale_f32_16x16x128_f8f6f4 v[134:137], v[2:9], v[206:213], v[134:137], v187, v188 op_sel_hi:[0,0,0]
	v_mfma_scale_f32_16x16x128_f8f6f4 v[126:129], v[10:17], v[206:213], v[126:129], v187, v188 op_sel_hi:[0,0,0]
	v_mfma_scale_f32_16x16x128_f8f6f4 v[118:121], v[2:9], v[220:227], v[118:121], v187, v188 op_sel_hi:[0,0,0]
	v_mfma_scale_f32_16x16x128_f8f6f4 v[110:113], v[10:17], v[220:227], v[110:113], v187, v188 op_sel_hi:[0,0,0]
	v_mfma_scale_f32_16x16x128_f8f6f4 v[146:149], v[18:25], v[190:197], v[146:149], v187, v188 op_sel_hi:[0,0,0]
	v_mfma_scale_f32_16x16x128_f8f6f4 v[138:141], v[26:33], v[190:197], v[138:141], v187, v188 op_sel_hi:[0,0,0]
	v_mfma_scale_f32_16x16x128_f8f6f4 v[130:133], v[18:25], v[198:205], v[130:133], v187, v188 op_sel_hi:[0,0,0]
	v_mfma_scale_f32_16x16x128_f8f6f4 v[122:125], v[26:33], v[198:205], v[122:125], v187, v188 op_sel_hi:[0,0,0]
	v_mfma_scale_f32_16x16x128_f8f6f4 v[114:117], v[18:25], v[206:213], v[114:117], v187, v188 op_sel_hi:[0,0,0]
	v_mfma_scale_f32_16x16x128_f8f6f4 v[106:109], v[26:33], v[206:213], v[106:109], v187, v188 op_sel_hi:[0,0,0]
	v_mfma_scale_f32_16x16x128_f8f6f4 v[102:105], v[18:25], v[220:227], v[102:105], v187, v188 op_sel_hi:[0,0,0]
	v_mfma_scale_f32_16x16x128_f8f6f4 v[98:101], v[26:33], v[220:227], v[98:101], v187, v188 op_sel_hi:[0,0,0]
	s_barrier
	s_add_i32 s26, s74, s80
	v_lshl_add_u64 v[214:215], v[176:177], 0, s[16:17]
	s_mov_b32 m0, s26
	ds_read_b128 v[190:193], v186 offset:49152
	ds_read_b128 v[194:197], v186 offset:50176
	ds_read_b128 v[198:201], v186 offset:51200
	ds_read_b128 v[202:205], v186 offset:52224
	ds_read_b128 v[206:209], v186 offset:53248
	ds_read_b128 v[210:213], v186 offset:54272
	ds_read_b128 v[220:223], v186 offset:55296
	ds_read_b128 v[224:227], v186 offset:56320
	global_load_lds_dwordx4 v[214:215], off
	v_lshl_add_u64 v[214:215], v[176:177], 0, s[18:19]
	s_add_i32 m0, s26, 0x2000
	s_add_i32 s26, s75, s80
	global_load_lds_dwordx4 v[214:215], off
	v_lshl_add_u64 v[214:215], v[176:177], 0, s[22:23]
	s_mov_b32 m0, s26
	v_lshl_add_u64 v[176:177], v[176:177], 0, s[24:25]
	global_load_lds_dwordx4 v[214:215], off
	s_add_i32 m0, s26, 0x2000
	s_nop 0
	global_load_lds_dwordx4 v[176:177], off
	v_lshl_add_u64 v[176:177], v[178:179], 0, s[20:21]
	s_mov_b32 m0, s86
	s_nop 0
	global_load_lds_dwordx4 v[176:177], off
	v_lshl_add_u64 v[176:177], v[180:181], 0, s[20:21]
	s_mov_b32 m0, s87
	s_nop 0
	global_load_lds_dwordx4 v[176:177], off
	s_waitcnt vmcnt(8)
	s_waitcnt lgkmcnt(0)
	s_barrier
	v_mfma_scale_f32_16x16x128_f8f6f4 v[94:97], v[2:9], v[190:197], v[94:97], v187, v188 op_sel_hi:[0,0,0]
	s_add_i32 s94, s94, 2
	s_add_u32 s92, s92, 0x10000
	s_addc_u32 s93, s93, 0
	s_add_u32 s70, s70, 0x100
	s_addc_u32 s71, s71, 0
	s_cmp_gt_u32 s94, 13
	v_mfma_scale_f32_16x16x128_f8f6f4 v[90:93], v[10:17], v[190:197], v[90:93], v187, v188 op_sel_hi:[0,0,0]
	v_mfma_scale_f32_16x16x128_f8f6f4 v[86:89], v[2:9], v[198:205], v[86:89], v187, v188 op_sel_hi:[0,0,0]
	v_mfma_scale_f32_16x16x128_f8f6f4 v[78:81], v[10:17], v[198:205], v[78:81], v187, v188 op_sel_hi:[0,0,0]
	v_mfma_scale_f32_16x16x128_f8f6f4 v[70:73], v[2:9], v[206:213], v[70:73], v187, v188 op_sel_hi:[0,0,0]
	v_mfma_scale_f32_16x16x128_f8f6f4 v[62:65], v[10:17], v[206:213], v[62:65], v187, v188 op_sel_hi:[0,0,0]
	v_mfma_scale_f32_16x16x128_f8f6f4 v[54:57], v[2:9], v[220:227], v[54:57], v187, v188 op_sel_hi:[0,0,0]
	v_mfma_scale_f32_16x16x128_f8f6f4 v[46:49], v[10:17], v[220:227], v[46:49], v187, v188 op_sel_hi:[0,0,0]
	v_mfma_scale_f32_16x16x128_f8f6f4 v[82:85], v[18:25], v[190:197], v[82:85], v187, v188 op_sel_hi:[0,0,0]
	v_mfma_scale_f32_16x16x128_f8f6f4 v[74:77], v[26:33], v[190:197], v[74:77], v187, v188 op_sel_hi:[0,0,0]
	v_mfma_scale_f32_16x16x128_f8f6f4 v[66:69], v[18:25], v[198:205], v[66:69], v187, v188 op_sel_hi:[0,0,0]
	v_mfma_scale_f32_16x16x128_f8f6f4 v[58:61], v[26:33], v[198:205], v[58:61], v187, v188 op_sel_hi:[0,0,0]
	v_mfma_scale_f32_16x16x128_f8f6f4 v[50:53], v[18:25], v[206:213], v[50:53], v187, v188 op_sel_hi:[0,0,0]
	v_mfma_scale_f32_16x16x128_f8f6f4 v[42:45], v[26:33], v[206:213], v[42:45], v187, v188 op_sel_hi:[0,0,0]
	v_mfma_scale_f32_16x16x128_f8f6f4 v[38:41], v[18:25], v[220:227], v[38:41], v187, v188 op_sel_hi:[0,0,0]
	v_mfma_scale_f32_16x16x128_f8f6f4 v[34:37], v[26:33], v[220:227], v[34:37], v187, v188 op_sel_hi:[0,0,0]
	s_barrier
	s_cbranch_scc0 .LBB0_285
	s_and_b64 vcc, exec, s[40:41]
	s_cbranch_vccz .LBB0_288
	s_barrier

.LBB0_660:
	ds_read_b128 v[130:133], v222
	ds_read_b128 v[134:137], v222 offset:1024
	ds_read_b128 v[138:141], v222 offset:2048
	ds_read_b128 v[142:145], v222 offset:3072
	ds_read_b128 v[146:149], v223
	ds_read_b128 v[150:153], v223 offset:1024
	ds_read_b128 v[154:157], v223 offset:2048
	ds_read_b128 v[158:161], v223 offset:3072
	s_add_u32 s26, s58, 0xfff80080
	s_addc_u32 s27, s59, -1
	s_cmp_eq_u32 s80, 28
	s_cselect_b32 s61, s45, s27
	s_cselect_b32 s60, s72, s26
	s_cselect_b32 s27, s41, s75
	s_cselect_b32 s26, s73, s74
	v_lshl_add_u64 v[208:209], s[58:59], 0, v[200:201]
	s_add_i32 m0, s57, 0xc000
	ds_read_b128 v[162:165], v224
	ds_read_b128 v[166:169], v224 offset:1024
	ds_read_b128 v[170:173], v224 offset:2048
	ds_read_b128 v[174:177], v224 offset:3072
	ds_read_b128 v[178:181], v224 offset:4096
	ds_read_b128 v[182:185], v224 offset:5120
	ds_read_b128 v[186:189], v224 offset:6144
	ds_read_b128 v[190:193], v224 offset:7168
	global_load_lds_dwordx4 v[208:209], off
	v_lshl_add_u64 v[208:209], s[58:59], 0, v[202:203]
	s_add_i32 m0, s57, 0xe000
	s_nop 0
	global_load_lds_dwordx4 v[208:209], off
	s_waitcnt vmcnt(8)
	s_waitcnt lgkmcnt(0)
	s_barrier
	v_mfma_f32_16x16x32_bf16 v[126:129], v[130:133], v[162:165], v[126:129]
	v_mfma_f32_16x16x32_bf16 v[122:125], v[138:141], v[162:165], v[122:125]
	v_mfma_f32_16x16x32_bf16 v[118:121], v[130:133], v[170:173], v[118:121]
	v_mfma_f32_16x16x32_bf16 v[114:117], v[138:141], v[170:173], v[114:117]
	v_mfma_f32_16x16x32_bf16 v[110:113], v[130:133], v[178:181], v[110:113]
	v_mfma_f32_16x16x32_bf16 v[102:105], v[138:141], v[178:181], v[102:105]
	v_mfma_f32_16x16x32_bf16 v[94:97], v[130:133], v[186:189], v[94:97]
	v_mfma_f32_16x16x32_bf16 v[74:77], v[138:141], v[186:189], v[74:77]
	v_mfma_f32_16x16x32_bf16 v[126:129], v[134:137], v[166:169], v[126:129]
	v_mfma_f32_16x16x32_bf16 v[122:125], v[142:145], v[166:169], v[122:125]
	v_mfma_f32_16x16x32_bf16 v[118:121], v[134:137], v[174:177], v[118:121]
	v_mfma_f32_16x16x32_bf16 v[114:117], v[142:145], v[174:177], v[114:117]
	v_mfma_f32_16x16x32_bf16 v[110:113], v[134:137], v[182:185], v[110:113]
	v_mfma_f32_16x16x32_bf16 v[102:105], v[142:145], v[182:185], v[102:105]
	v_mfma_f32_16x16x32_bf16 v[94:97], v[134:137], v[190:193], v[94:97]
	v_mfma_f32_16x16x32_bf16 v[74:77], v[142:145], v[190:193], v[74:77]
	v_mfma_f32_16x16x32_bf16 v[106:109], v[146:149], v[162:165], v[106:109]
	v_mfma_f32_16x16x32_bf16 v[98:101], v[154:157], v[162:165], v[98:101]
	v_mfma_f32_16x16x32_bf16 v[90:93], v[146:149], v[170:173], v[90:93]
	v_mfma_f32_16x16x32_bf16 v[86:89], v[154:157], v[170:173], v[86:89]
	v_mfma_f32_16x16x32_bf16 v[82:85], v[146:149], v[178:181], v[82:85]
	v_mfma_f32_16x16x32_bf16 v[78:81], v[154:157], v[178:181], v[78:81]
	v_mfma_f32_16x16x32_bf16 v[70:73], v[146:149], v[186:189], v[70:73]
	v_mfma_f32_16x16x32_bf16 v[66:69], v[154:157], v[186:189], v[66:69]
	v_mfma_f32_16x16x32_bf16 v[106:109], v[150:153], v[166:169], v[106:109]
	v_mfma_f32_16x16x32_bf16 v[98:101], v[158:161], v[166:169], v[98:101]
	v_mfma_f32_16x16x32_bf16 v[90:93], v[150:153], v[174:177], v[90:93]
	v_mfma_f32_16x16x32_bf16 v[86:89], v[158:161], v[174:177], v[86:89]
	v_mfma_f32_16x16x32_bf16 v[82:85], v[150:153], v[182:185], v[82:85]
	v_mfma_f32_16x16x32_bf16 v[78:81], v[158:161], v[182:185], v[78:81]
	v_mfma_f32_16x16x32_bf16 v[70:73], v[150:153], v[190:193], v[70:73]
	v_mfma_f32_16x16x32_bf16 v[66:69], v[158:161], v[190:193], v[66:69]
	s_barrier
	v_lshl_add_u64 v[208:209], s[26:27], 0, v[194:195]
	s_add_i32 s26, s70, s35
	s_mov_b32 m0, s26
	ds_read_b128 v[162:165], v224 offset:16384
	ds_read_b128 v[166:169], v224 offset:17408
	ds_read_b128 v[170:173], v224 offset:18432
	ds_read_b128 v[174:177], v224 offset:19456
	ds_read_b128 v[178:181], v224 offset:20480
	ds_read_b128 v[182:185], v224 offset:21504
	ds_read_b128 v[186:189], v224 offset:22528
	ds_read_b128 v[190:193], v224 offset:23552
	global_load_lds_dwordx4 v[208:209], off
	v_lshl_add_u64 v[210:211], v[208:209], 0, s[6:7]
	s_add_i32 m0, s26, 0x2000
	s_add_i32 s26, s71, s35
	global_load_lds_dwordx4 v[210:211], off
	v_lshl_add_u64 v[210:211], v[208:209], 0, s[8:9]
	s_mov_b32 m0, s26
	v_lshl_add_u64 v[212:213], s[60:61], 0, v[198:199]
	global_load_lds_dwordx4 v[210:211], off
	v_lshl_add_u64 v[210:211], v[208:209], 0, s[10:11]
	s_add_i32 m0, s26, 0x2000
	s_nop 0
	global_load_lds_dwordx4 v[210:211], off
	v_lshl_add_u64 v[210:211], s[60:61], 0, v[196:197]
	s_mov_b32 m0, s57
	s_nop 0
	global_load_lds_dwordx4 v[210:211], off
	s_mov_b32 m0, s63
	s_nop 0
	global_load_lds_dwordx4 v[212:213], off
	s_waitcnt vmcnt(8)
	s_waitcnt lgkmcnt(0)
	s_barrier
	v_mfma_f32_16x16x32_bf16 v[62:65], v[130:133], v[162:165], v[62:65]
	v_mfma_f32_16x16x32_bf16 v[58:61], v[138:141], v[162:165], v[58:61]
	v_mfma_f32_16x16x32_bf16 v[54:57], v[130:133], v[170:173], v[54:57]
	v_mfma_f32_16x16x32_bf16 v[50:53], v[138:141], v[170:173], v[50:53]
	v_mfma_f32_16x16x32_bf16 v[46:49], v[130:133], v[178:181], v[46:49]
	v_mfma_f32_16x16x32_bf16 v[38:41], v[138:141], v[178:181], v[38:41]
	v_mfma_f32_16x16x32_bf16 v[30:33], v[130:133], v[186:189], v[30:33]
	v_mfma_f32_16x16x32_bf16 v[10:13], v[138:141], v[186:189], v[10:13]
	v_mfma_f32_16x16x32_bf16 v[62:65], v[134:137], v[166:169], v[62:65]
	v_mfma_f32_16x16x32_bf16 v[58:61], v[142:145], v[166:169], v[58:61]
	v_mfma_f32_16x16x32_bf16 v[54:57], v[134:137], v[174:177], v[54:57]
	v_mfma_f32_16x16x32_bf16 v[50:53], v[142:145], v[174:177], v[50:53]
	v_mfma_f32_16x16x32_bf16 v[46:49], v[134:137], v[182:185], v[46:49]
	v_mfma_f32_16x16x32_bf16 v[38:41], v[142:145], v[182:185], v[38:41]
	v_mfma_f32_16x16x32_bf16 v[30:33], v[134:137], v[190:193], v[30:33]
	v_mfma_f32_16x16x32_bf16 v[10:13], v[142:145], v[190:193], v[10:13]
	v_mfma_f32_16x16x32_bf16 v[42:45], v[146:149], v[162:165], v[42:45]
	v_mfma_f32_16x16x32_bf16 v[34:37], v[154:157], v[162:165], v[34:37]
	v_mfma_f32_16x16x32_bf16 v[26:29], v[146:149], v[170:173], v[26:29]
	v_mfma_f32_16x16x32_bf16 v[22:25], v[154:157], v[170:173], v[22:25]
	v_mfma_f32_16x16x32_bf16 v[18:21], v[146:149], v[178:181], v[18:21]
	v_mfma_f32_16x16x32_bf16 v[14:17], v[154:157], v[178:181], v[14:17]
	v_mfma_f32_16x16x32_bf16 v[6:9], v[146:149], v[186:189], v[6:9]
	v_mfma_f32_16x16x32_bf16 v[2:5], v[154:157], v[186:189], v[2:5]
	v_mfma_f32_16x16x32_bf16 v[42:45], v[150:153], v[166:169], v[42:45]
	v_mfma_f32_16x16x32_bf16 v[34:37], v[158:161], v[166:169], v[34:37]
	v_mfma_f32_16x16x32_bf16 v[26:29], v[150:153], v[174:177], v[26:29]
	v_mfma_f32_16x16x32_bf16 v[22:25], v[158:161], v[174:177], v[22:25]
	v_mfma_f32_16x16x32_bf16 v[18:21], v[150:153], v[182:185], v[18:21]
	v_mfma_f32_16x16x32_bf16 v[14:17], v[158:161], v[182:185], v[14:17]
	v_mfma_f32_16x16x32_bf16 v[6:9], v[150:153], v[190:193], v[6:9]
	v_mfma_f32_16x16x32_bf16 v[2:5], v[158:161], v[190:193], v[2:5]
	s_barrier
	s_add_i32 s81, 0, 0x18000
	s_add_i32 s82, 0, 0x1c000
	v_add_u32_e32 v142, s81, v220
	v_add_u32_e32 v158, s82, v220
	ds_read_b128 v[130:133], v142
	ds_read_b128 v[134:137], v142 offset:1024
	ds_read_b128 v[138:141], v142 offset:2048
	ds_read_b128 v[142:145], v142 offset:3072
	ds_read_b128 v[146:149], v158
	ds_read_b128 v[150:153], v158 offset:1024
	ds_read_b128 v[154:157], v158 offset:2048
	ds_read_b128 v[158:161], v158 offset:3072
	s_add_u32 s26, s60, 0x80000
	s_addc_u32 s27, s61, 0
	s_mov_b32 m0, s64
	v_lshl_add_u64 v[214:215], s[26:27], 0, v[196:197]
	ds_read_b128 v[162:165], v224 offset:32768
	ds_read_b128 v[166:169], v224 offset:33792
	ds_read_b128 v[170:173], v224 offset:34816
	ds_read_b128 v[174:177], v224 offset:35840
	ds_read_b128 v[178:181], v224 offset:36864
	ds_read_b128 v[182:185], v224 offset:37888
	ds_read_b128 v[186:189], v224 offset:38912
	ds_read_b128 v[190:193], v224 offset:39936
	global_load_lds_dwordx4 v[214:215], off
	v_lshl_add_u64 v[214:215], s[26:27], 0, v[198:199]
	s_mov_b32 m0, s65
	s_nop 0
	global_load_lds_dwordx4 v[214:215], off
	s_waitcnt vmcnt(8)
	s_waitcnt lgkmcnt(0)
	s_barrier
	v_mfma_f32_16x16x32_bf16 v[126:129], v[130:133], v[162:165], v[126:129]
	v_mfma_f32_16x16x32_bf16 v[122:125], v[138:141], v[162:165], v[122:125]
	v_mfma_f32_16x16x32_bf16 v[118:121], v[130:133], v[170:173], v[118:121]
	v_mfma_f32_16x16x32_bf16 v[114:117], v[138:141], v[170:173], v[114:117]
	v_mfma_f32_16x16x32_bf16 v[110:113], v[130:133], v[178:181], v[110:113]
	v_mfma_f32_16x16x32_bf16 v[102:105], v[138:141], v[178:181], v[102:105]
	v_mfma_f32_16x16x32_bf16 v[94:97], v[130:133], v[186:189], v[94:97]
	v_mfma_f32_16x16x32_bf16 v[74:77], v[138:141], v[186:189], v[74:77]
	v_mfma_f32_16x16x32_bf16 v[126:129], v[134:137], v[166:169], v[126:129]
	v_mfma_f32_16x16x32_bf16 v[122:125], v[142:145], v[166:169], v[122:125]
	v_mfma_f32_16x16x32_bf16 v[118:121], v[134:137], v[174:177], v[118:121]
	v_mfma_f32_16x16x32_bf16 v[114:117], v[142:145], v[174:177], v[114:117]
	v_mfma_f32_16x16x32_bf16 v[110:113], v[134:137], v[182:185], v[110:113]
	v_mfma_f32_16x16x32_bf16 v[102:105], v[142:145], v[182:185], v[102:105]
	v_mfma_f32_16x16x32_bf16 v[94:97], v[134:137], v[190:193], v[94:97]
	v_mfma_f32_16x16x32_bf16 v[74:77], v[142:145], v[190:193], v[74:77]
	v_mfma_f32_16x16x32_bf16 v[106:109], v[146:149], v[162:165], v[106:109]
	v_mfma_f32_16x16x32_bf16 v[98:101], v[154:157], v[162:165], v[98:101]
	v_mfma_f32_16x16x32_bf16 v[90:93], v[146:149], v[170:173], v[90:93]
	v_mfma_f32_16x16x32_bf16 v[86:89], v[154:157], v[170:173], v[86:89]
	v_mfma_f32_16x16x32_bf16 v[82:85], v[146:149], v[178:181], v[82:85]
	v_mfma_f32_16x16x32_bf16 v[78:81], v[154:157], v[178:181], v[78:81]
	v_mfma_f32_16x16x32_bf16 v[70:73], v[146:149], v[186:189], v[70:73]
	v_mfma_f32_16x16x32_bf16 v[66:69], v[154:157], v[186:189], v[66:69]
	v_mfma_f32_16x16x32_bf16 v[106:109], v[150:153], v[166:169], v[106:109]
	v_mfma_f32_16x16x32_bf16 v[98:101], v[158:161], v[166:169], v[98:101]
	v_mfma_f32_16x16x32_bf16 v[90:93], v[150:153], v[174:177], v[90:93]
	v_mfma_f32_16x16x32_bf16 v[86:89], v[158:161], v[174:177], v[86:89]
	v_mfma_f32_16x16x32_bf16 v[82:85], v[150:153], v[182:185], v[82:85]
	v_mfma_f32_16x16x32_bf16 v[78:81], v[158:161], v[182:185], v[78:81]
	v_mfma_f32_16x16x32_bf16 v[70:73], v[150:153], v[190:193], v[70:73]
	v_mfma_f32_16x16x32_bf16 v[66:69], v[158:161], v[190:193], v[66:69]
	s_barrier
	s_add_i32 s26, s81, s35
	v_lshl_add_u64 v[214:215], v[208:209], 0, s[14:15]
	s_mov_b32 m0, s26
	ds_read_b128 v[162:165], v224 offset:49152
	ds_read_b128 v[166:169], v224 offset:50176
	ds_read_b128 v[170:173], v224 offset:51200
	ds_read_b128 v[174:177], v224 offset:52224
	ds_read_b128 v[178:181], v224 offset:53248
	ds_read_b128 v[182:185], v224 offset:54272
	ds_read_b128 v[186:189], v224 offset:55296
	ds_read_b128 v[190:193], v224 offset:56320
	global_load_lds_dwordx4 v[214:215], off
	v_lshl_add_u64 v[214:215], v[208:209], 0, s[16:17]
	s_add_i32 m0, s26, 0x2000
	s_add_i32 s26, s82, s35
	global_load_lds_dwordx4 v[214:215], off
	v_lshl_add_u64 v[214:215], v[208:209], 0, s[20:21]
	s_mov_b32 m0, s26
	v_lshl_add_u64 v[208:209], v[208:209], 0, s[22:23]
	global_load_lds_dwordx4 v[214:215], off
	s_add_i32 m0, s26, 0x2000
	s_nop 0
	global_load_lds_dwordx4 v[208:209], off
	v_lshl_add_u64 v[208:209], v[210:211], 0, s[18:19]
	s_mov_b32 m0, s67
	s_nop 0
	global_load_lds_dwordx4 v[208:209], off
	v_lshl_add_u64 v[208:209], v[212:213], 0, s[18:19]
	s_mov_b32 m0, s68
	s_nop 0
	global_load_lds_dwordx4 v[208:209], off
	s_waitcnt vmcnt(8)
	s_waitcnt lgkmcnt(0)
	s_barrier
	v_mfma_f32_16x16x32_bf16 v[62:65], v[130:133], v[162:165], v[62:65]
	s_add_i32 s80, s80, 2
	s_add_u32 s74, s74, 0x10000
	s_addc_u32 s75, s75, 0
	s_add_u32 s58, s58, 0x100
	s_addc_u32 s59, s59, 0
	s_cmp_gt_u32 s80, 29
	v_mfma_f32_16x16x32_bf16 v[58:61], v[138:141], v[162:165], v[58:61]
	v_mfma_f32_16x16x32_bf16 v[54:57], v[130:133], v[170:173], v[54:57]
	v_mfma_f32_16x16x32_bf16 v[50:53], v[138:141], v[170:173], v[50:53]
	v_mfma_f32_16x16x32_bf16 v[46:49], v[130:133], v[178:181], v[46:49]
	v_mfma_f32_16x16x32_bf16 v[38:41], v[138:141], v[178:181], v[38:41]
	v_mfma_f32_16x16x32_bf16 v[30:33], v[130:133], v[186:189], v[30:33]
	v_mfma_f32_16x16x32_bf16 v[10:13], v[138:141], v[186:189], v[10:13]
	v_mfma_f32_16x16x32_bf16 v[62:65], v[134:137], v[166:169], v[62:65]
	v_mfma_f32_16x16x32_bf16 v[58:61], v[142:145], v[166:169], v[58:61]
	v_mfma_f32_16x16x32_bf16 v[54:57], v[134:137], v[174:177], v[54:57]
	v_mfma_f32_16x16x32_bf16 v[50:53], v[142:145], v[174:177], v[50:53]
	v_mfma_f32_16x16x32_bf16 v[46:49], v[134:137], v[182:185], v[46:49]
	v_mfma_f32_16x16x32_bf16 v[38:41], v[142:145], v[182:185], v[38:41]
	v_mfma_f32_16x16x32_bf16 v[30:33], v[134:137], v[190:193], v[30:33]
	v_mfma_f32_16x16x32_bf16 v[10:13], v[142:145], v[190:193], v[10:13]
	v_mfma_f32_16x16x32_bf16 v[42:45], v[146:149], v[162:165], v[42:45]
	v_mfma_f32_16x16x32_bf16 v[34:37], v[154:157], v[162:165], v[34:37]
	v_mfma_f32_16x16x32_bf16 v[26:29], v[146:149], v[170:173], v[26:29]
	v_mfma_f32_16x16x32_bf16 v[22:25], v[154:157], v[170:173], v[22:25]
	v_mfma_f32_16x16x32_bf16 v[18:21], v[146:149], v[178:181], v[18:21]
	v_mfma_f32_16x16x32_bf16 v[14:17], v[154:157], v[178:181], v[14:17]
	v_mfma_f32_16x16x32_bf16 v[6:9], v[146:149], v[186:189], v[6:9]
	v_mfma_f32_16x16x32_bf16 v[2:5], v[154:157], v[186:189], v[2:5]
	v_mfma_f32_16x16x32_bf16 v[42:45], v[150:153], v[166:169], v[42:45]
	v_mfma_f32_16x16x32_bf16 v[34:37], v[158:161], v[166:169], v[34:37]
	v_mfma_f32_16x16x32_bf16 v[26:29], v[150:153], v[174:177], v[26:29]
	v_mfma_f32_16x16x32_bf16 v[22:25], v[158:161], v[174:177], v[22:25]
	v_mfma_f32_16x16x32_bf16 v[18:21], v[150:153], v[182:185], v[18:21]
	v_mfma_f32_16x16x32_bf16 v[14:17], v[158:161], v[182:185], v[14:17]
	v_mfma_f32_16x16x32_bf16 v[6:9], v[150:153], v[190:193], v[6:9]
	v_mfma_f32_16x16x32_bf16 v[2:5], v[158:161], v[190:193], v[2:5]
	s_barrier
	s_cbranch_scc0 .LBB0_660
	s_and_b64 vcc, exec, s[24:25]
	s_cbranch_vccz .LBB0_663
	s_barrier

.LBB0_783:
	ds_read_b128 v[144:147], v151
	ds_read_b128 v[156:159], v151 offset:1024
	ds_read_b128 v[160:163], v151 offset:2048
	ds_read_b128 v[164:167], v151 offset:3072
	ds_read_b128 v[168:171], v152
	ds_read_b128 v[172:175], v152 offset:1024
	ds_read_b128 v[176:179], v152 offset:2048
	ds_read_b128 v[180:183], v152 offset:3072
	s_add_u32 s26, s62, 0xfff80080
	s_addc_u32 s27, s63, -1
	s_cmp_eq_u32 s85, 28
	s_cselect_b32 s65, s55, s27
	s_cselect_b32 s64, s81, s26
	s_cselect_b32 s27, s53, s84
	s_cselect_b32 s26, s82, s83
	v_lshl_add_u64 v[216:217], s[62:63], 0, v[136:137]
	s_add_i32 m0, s61, 0xc000
	ds_read_b128 v[184:187], v153
	ds_read_b128 v[188:191], v153 offset:1024
	ds_read_b128 v[192:195], v153 offset:2048
	ds_read_b128 v[196:199], v153 offset:3072
	ds_read_b128 v[200:203], v153 offset:4096
	ds_read_b128 v[204:207], v153 offset:5120
	ds_read_b128 v[208:211], v153 offset:6144
	ds_read_b128 v[212:215], v153 offset:7168
	global_load_lds_dwordx4 v[216:217], off
	v_lshl_add_u64 v[216:217], s[62:63], 0, v[138:139]
	s_add_i32 m0, s61, 0xe000
	s_nop 0
	global_load_lds_dwordx4 v[216:217], off
	s_waitcnt vmcnt(8)
	s_waitcnt lgkmcnt(0)
	s_barrier
	v_mfma_f32_16x16x32_bf16 v[126:129], v[144:147], v[184:187], v[126:129]
	v_mfma_f32_16x16x32_bf16 v[118:121], v[160:163], v[184:187], v[118:121]
	v_mfma_f32_16x16x32_bf16 v[110:113], v[144:147], v[192:195], v[110:113]
	v_mfma_f32_16x16x32_bf16 v[102:105], v[160:163], v[192:195], v[102:105]
	v_mfma_f32_16x16x32_bf16 v[94:97], v[144:147], v[200:203], v[94:97]
	v_mfma_f32_16x16x32_bf16 v[86:89], v[160:163], v[200:203], v[86:89]
	v_mfma_f32_16x16x32_bf16 v[78:81], v[144:147], v[208:211], v[78:81]
	v_mfma_f32_16x16x32_bf16 v[70:73], v[160:163], v[208:211], v[70:73]
	v_mfma_f32_16x16x32_bf16 v[126:129], v[156:159], v[188:191], v[126:129]
	v_mfma_f32_16x16x32_bf16 v[118:121], v[164:167], v[188:191], v[118:121]
	v_mfma_f32_16x16x32_bf16 v[110:113], v[156:159], v[196:199], v[110:113]
	v_mfma_f32_16x16x32_bf16 v[102:105], v[164:167], v[196:199], v[102:105]
	v_mfma_f32_16x16x32_bf16 v[94:97], v[156:159], v[204:207], v[94:97]
	v_mfma_f32_16x16x32_bf16 v[86:89], v[164:167], v[204:207], v[86:89]
	v_mfma_f32_16x16x32_bf16 v[78:81], v[156:159], v[212:215], v[78:81]
	v_mfma_f32_16x16x32_bf16 v[70:73], v[164:167], v[212:215], v[70:73]
	v_mfma_f32_16x16x32_bf16 v[122:125], v[168:171], v[184:187], v[122:125]
	v_mfma_f32_16x16x32_bf16 v[114:117], v[176:179], v[184:187], v[114:117]
	v_mfma_f32_16x16x32_bf16 v[106:109], v[168:171], v[192:195], v[106:109]
	v_mfma_f32_16x16x32_bf16 v[98:101], v[176:179], v[192:195], v[98:101]
	v_mfma_f32_16x16x32_bf16 v[90:93], v[168:171], v[200:203], v[90:93]
	v_mfma_f32_16x16x32_bf16 v[82:85], v[176:179], v[200:203], v[82:85]
	v_mfma_f32_16x16x32_bf16 v[74:77], v[168:171], v[208:211], v[74:77]
	v_mfma_f32_16x16x32_bf16 v[66:69], v[176:179], v[208:211], v[66:69]
	v_mfma_f32_16x16x32_bf16 v[122:125], v[172:175], v[188:191], v[122:125]
	v_mfma_f32_16x16x32_bf16 v[114:117], v[180:183], v[188:191], v[114:117]
	v_mfma_f32_16x16x32_bf16 v[106:109], v[172:175], v[196:199], v[106:109]
	v_mfma_f32_16x16x32_bf16 v[98:101], v[180:183], v[196:199], v[98:101]
	v_mfma_f32_16x16x32_bf16 v[90:93], v[172:175], v[204:207], v[90:93]
	v_mfma_f32_16x16x32_bf16 v[82:85], v[180:183], v[204:207], v[82:85]
	v_mfma_f32_16x16x32_bf16 v[74:77], v[172:175], v[212:215], v[74:77]
	v_mfma_f32_16x16x32_bf16 v[66:69], v[180:183], v[212:215], v[66:69]
	s_barrier
	v_lshl_add_u64 v[216:217], s[26:27], 0, v[130:131]
	s_add_i32 s26, s73, s35
	s_mov_b32 m0, s26
	ds_read_b128 v[184:187], v153 offset:16384
	ds_read_b128 v[188:191], v153 offset:17408
	ds_read_b128 v[192:195], v153 offset:18432
	ds_read_b128 v[196:199], v153 offset:19456
	ds_read_b128 v[200:203], v153 offset:20480
	ds_read_b128 v[204:207], v153 offset:21504
	ds_read_b128 v[208:211], v153 offset:22528
	ds_read_b128 v[212:215], v153 offset:23552
	global_load_lds_dwordx4 v[216:217], off
	v_lshl_add_u64 v[220:221], v[216:217], 0, s[6:7]
	s_add_i32 m0, s26, 0x2000
	s_add_i32 s26, s74, s35
	global_load_lds_dwordx4 v[220:221], off
	v_lshl_add_u64 v[220:221], v[216:217], 0, s[8:9]
	s_mov_b32 m0, s26
	v_lshl_add_u64 v[222:223], s[64:65], 0, v[134:135]
	global_load_lds_dwordx4 v[220:221], off
	v_lshl_add_u64 v[220:221], v[216:217], 0, s[10:11]
	s_add_i32 m0, s26, 0x2000
	s_nop 0
	global_load_lds_dwordx4 v[220:221], off
	v_lshl_add_u64 v[220:221], s[64:65], 0, v[132:133]
	s_mov_b32 m0, s61
	s_nop 0
	global_load_lds_dwordx4 v[220:221], off
	s_mov_b32 m0, s66
	s_nop 0
	global_load_lds_dwordx4 v[222:223], off
	s_waitcnt vmcnt(8)
	s_waitcnt lgkmcnt(0)
	s_barrier
	v_mfma_f32_16x16x32_bf16 v[62:65], v[144:147], v[184:187], v[62:65]
	v_mfma_f32_16x16x32_bf16 v[54:57], v[160:163], v[184:187], v[54:57]
	v_mfma_f32_16x16x32_bf16 v[46:49], v[144:147], v[192:195], v[46:49]
	v_mfma_f32_16x16x32_bf16 v[38:41], v[160:163], v[192:195], v[38:41]
	v_mfma_f32_16x16x32_bf16 v[30:33], v[144:147], v[200:203], v[30:33]
	v_mfma_f32_16x16x32_bf16 v[22:25], v[160:163], v[200:203], v[22:25]
	v_mfma_f32_16x16x32_bf16 v[14:17], v[144:147], v[208:211], v[14:17]
	v_mfma_f32_16x16x32_bf16 v[6:9], v[160:163], v[208:211], v[6:9]
	v_mfma_f32_16x16x32_bf16 v[62:65], v[156:159], v[188:191], v[62:65]
	v_mfma_f32_16x16x32_bf16 v[54:57], v[164:167], v[188:191], v[54:57]
	v_mfma_f32_16x16x32_bf16 v[46:49], v[156:159], v[196:199], v[46:49]
	v_mfma_f32_16x16x32_bf16 v[38:41], v[164:167], v[196:199], v[38:41]
	v_mfma_f32_16x16x32_bf16 v[30:33], v[156:159], v[204:207], v[30:33]
	v_mfma_f32_16x16x32_bf16 v[22:25], v[164:167], v[204:207], v[22:25]
	v_mfma_f32_16x16x32_bf16 v[14:17], v[156:159], v[212:215], v[14:17]
	v_mfma_f32_16x16x32_bf16 v[6:9], v[164:167], v[212:215], v[6:9]
	v_mfma_f32_16x16x32_bf16 v[58:61], v[168:171], v[184:187], v[58:61]
	v_mfma_f32_16x16x32_bf16 v[50:53], v[176:179], v[184:187], v[50:53]
	v_mfma_f32_16x16x32_bf16 v[42:45], v[168:171], v[192:195], v[42:45]
	v_mfma_f32_16x16x32_bf16 v[34:37], v[176:179], v[192:195], v[34:37]
	v_mfma_f32_16x16x32_bf16 v[26:29], v[168:171], v[200:203], v[26:29]
	v_mfma_f32_16x16x32_bf16 v[18:21], v[176:179], v[200:203], v[18:21]
	v_mfma_f32_16x16x32_bf16 v[10:13], v[168:171], v[208:211], v[10:13]
	v_mfma_f32_16x16x32_bf16 v[2:5], v[176:179], v[208:211], v[2:5]
	v_mfma_f32_16x16x32_bf16 v[58:61], v[172:175], v[188:191], v[58:61]
	v_mfma_f32_16x16x32_bf16 v[50:53], v[180:183], v[188:191], v[50:53]
	v_mfma_f32_16x16x32_bf16 v[42:45], v[172:175], v[196:199], v[42:45]
	v_mfma_f32_16x16x32_bf16 v[34:37], v[180:183], v[196:199], v[34:37]
	v_mfma_f32_16x16x32_bf16 v[26:29], v[172:175], v[204:207], v[26:29]
	v_mfma_f32_16x16x32_bf16 v[18:21], v[180:183], v[204:207], v[18:21]
	v_mfma_f32_16x16x32_bf16 v[10:13], v[172:175], v[212:215], v[10:13]
	v_mfma_f32_16x16x32_bf16 v[2:5], v[180:183], v[212:215], v[2:5]
	s_barrier
	s_add_i32 s86, 0, 0x18000
	v_add_u32_e32 v155, s86, v149
	s_add_i32 s87, 0, 0x1c000
	ds_read_b128 v[144:147], v155
	ds_read_b128 v[156:159], v155 offset:1024
	ds_read_b128 v[160:163], v155 offset:2048
	ds_read_b128 v[164:167], v155 offset:3072
	v_add_u32_e32 v155, s87, v149
	ds_read_b128 v[168:171], v155
	ds_read_b128 v[172:175], v155 offset:1024
	ds_read_b128 v[176:179], v155 offset:2048
	ds_read_b128 v[180:183], v155 offset:3072
	s_add_u32 s26, s64, 0x80000
	s_addc_u32 s27, s65, 0
	s_mov_b32 m0, s67
	v_lshl_add_u64 v[224:225], s[26:27], 0, v[132:133]
	ds_read_b128 v[184:187], v153 offset:32768
	ds_read_b128 v[188:191], v153 offset:33792
	ds_read_b128 v[192:195], v153 offset:34816
	ds_read_b128 v[196:199], v153 offset:35840
	ds_read_b128 v[200:203], v153 offset:36864
	ds_read_b128 v[204:207], v153 offset:37888
	ds_read_b128 v[208:211], v153 offset:38912
	ds_read_b128 v[212:215], v153 offset:39936
	global_load_lds_dwordx4 v[224:225], off
	v_lshl_add_u64 v[224:225], s[26:27], 0, v[134:135]
	s_mov_b32 m0, s68
	s_nop 0
	global_load_lds_dwordx4 v[224:225], off
	s_waitcnt vmcnt(8)
	s_waitcnt lgkmcnt(0)
	s_barrier
	v_mfma_f32_16x16x32_bf16 v[126:129], v[144:147], v[184:187], v[126:129]
	v_mfma_f32_16x16x32_bf16 v[118:121], v[160:163], v[184:187], v[118:121]
	v_mfma_f32_16x16x32_bf16 v[110:113], v[144:147], v[192:195], v[110:113]
	v_mfma_f32_16x16x32_bf16 v[102:105], v[160:163], v[192:195], v[102:105]
	v_mfma_f32_16x16x32_bf16 v[94:97], v[144:147], v[200:203], v[94:97]
	v_mfma_f32_16x16x32_bf16 v[86:89], v[160:163], v[200:203], v[86:89]
	v_mfma_f32_16x16x32_bf16 v[78:81], v[144:147], v[208:211], v[78:81]
	v_mfma_f32_16x16x32_bf16 v[70:73], v[160:163], v[208:211], v[70:73]
	v_mfma_f32_16x16x32_bf16 v[126:129], v[156:159], v[188:191], v[126:129]
	v_mfma_f32_16x16x32_bf16 v[118:121], v[164:167], v[188:191], v[118:121]
	v_mfma_f32_16x16x32_bf16 v[110:113], v[156:159], v[196:199], v[110:113]
	v_mfma_f32_16x16x32_bf16 v[102:105], v[164:167], v[196:199], v[102:105]
	v_mfma_f32_16x16x32_bf16 v[94:97], v[156:159], v[204:207], v[94:97]
	v_mfma_f32_16x16x32_bf16 v[86:89], v[164:167], v[204:207], v[86:89]
	v_mfma_f32_16x16x32_bf16 v[78:81], v[156:159], v[212:215], v[78:81]
	v_mfma_f32_16x16x32_bf16 v[70:73], v[164:167], v[212:215], v[70:73]
	v_mfma_f32_16x16x32_bf16 v[122:125], v[168:171], v[184:187], v[122:125]
	v_mfma_f32_16x16x32_bf16 v[114:117], v[176:179], v[184:187], v[114:117]
	v_mfma_f32_16x16x32_bf16 v[106:109], v[168:171], v[192:195], v[106:109]
	v_mfma_f32_16x16x32_bf16 v[98:101], v[176:179], v[192:195], v[98:101]
	v_mfma_f32_16x16x32_bf16 v[90:93], v[168:171], v[200:203], v[90:93]
	v_mfma_f32_16x16x32_bf16 v[82:85], v[176:179], v[200:203], v[82:85]
	v_mfma_f32_16x16x32_bf16 v[74:77], v[168:171], v[208:211], v[74:77]
	v_mfma_f32_16x16x32_bf16 v[66:69], v[176:179], v[208:211], v[66:69]
	v_mfma_f32_16x16x32_bf16 v[122:125], v[172:175], v[188:191], v[122:125]
	v_mfma_f32_16x16x32_bf16 v[114:117], v[180:183], v[188:191], v[114:117]
	v_mfma_f32_16x16x32_bf16 v[106:109], v[172:175], v[196:199], v[106:109]
	v_mfma_f32_16x16x32_bf16 v[98:101], v[180:183], v[196:199], v[98:101]
	v_mfma_f32_16x16x32_bf16 v[90:93], v[172:175], v[204:207], v[90:93]
	v_mfma_f32_16x16x32_bf16 v[82:85], v[180:183], v[204:207], v[82:85]
	v_mfma_f32_16x16x32_bf16 v[74:77], v[172:175], v[212:215], v[74:77]
	v_mfma_f32_16x16x32_bf16 v[66:69], v[180:183], v[212:215], v[66:69]
	s_barrier
	s_add_i32 s26, s86, s35
	v_lshl_add_u64 v[224:225], v[216:217], 0, s[16:17]
	s_mov_b32 m0, s26
	ds_read_b128 v[184:187], v153 offset:49152
	ds_read_b128 v[188:191], v153 offset:50176
	ds_read_b128 v[192:195], v153 offset:51200
	ds_read_b128 v[196:199], v153 offset:52224
	ds_read_b128 v[200:203], v153 offset:53248
	ds_read_b128 v[204:207], v153 offset:54272
	ds_read_b128 v[208:211], v153 offset:55296
	ds_read_b128 v[212:215], v153 offset:56320
	global_load_lds_dwordx4 v[224:225], off
	v_lshl_add_u64 v[224:225], v[216:217], 0, s[18:19]
	s_add_i32 m0, s26, 0x2000
	s_add_i32 s26, s87, s35
	global_load_lds_dwordx4 v[224:225], off
	v_lshl_add_u64 v[224:225], v[216:217], 0, s[22:23]
	s_mov_b32 m0, s26
	v_lshl_add_u64 v[216:217], v[216:217], 0, s[24:25]
	global_load_lds_dwordx4 v[224:225], off
	s_add_i32 m0, s26, 0x2000
	s_nop 0
	global_load_lds_dwordx4 v[216:217], off
	v_lshl_add_u64 v[216:217], v[220:221], 0, s[20:21]
	s_mov_b32 m0, s70
	s_nop 0
	global_load_lds_dwordx4 v[216:217], off
	v_lshl_add_u64 v[216:217], v[222:223], 0, s[20:21]
	s_mov_b32 m0, s71
	s_nop 0
	global_load_lds_dwordx4 v[216:217], off
	s_waitcnt vmcnt(8)
	s_waitcnt lgkmcnt(0)
	s_barrier
	v_mfma_f32_16x16x32_bf16 v[62:65], v[144:147], v[184:187], v[62:65]
	s_add_i32 s85, s85, 2
	s_add_u32 s83, s83, 0x10000
	s_addc_u32 s84, s84, 0
	s_add_u32 s62, s62, 0x100
	s_addc_u32 s63, s63, 0
	s_cmp_gt_u32 s85, 29
	v_mfma_f32_16x16x32_bf16 v[54:57], v[160:163], v[184:187], v[54:57]
	v_mfma_f32_16x16x32_bf16 v[46:49], v[144:147], v[192:195], v[46:49]
	v_mfma_f32_16x16x32_bf16 v[38:41], v[160:163], v[192:195], v[38:41]
	v_mfma_f32_16x16x32_bf16 v[30:33], v[144:147], v[200:203], v[30:33]
	v_mfma_f32_16x16x32_bf16 v[22:25], v[160:163], v[200:203], v[22:25]
	v_mfma_f32_16x16x32_bf16 v[14:17], v[144:147], v[208:211], v[14:17]
	v_mfma_f32_16x16x32_bf16 v[6:9], v[160:163], v[208:211], v[6:9]
	v_mfma_f32_16x16x32_bf16 v[62:65], v[156:159], v[188:191], v[62:65]
	v_mfma_f32_16x16x32_bf16 v[54:57], v[164:167], v[188:191], v[54:57]
	v_mfma_f32_16x16x32_bf16 v[46:49], v[156:159], v[196:199], v[46:49]
	v_mfma_f32_16x16x32_bf16 v[38:41], v[164:167], v[196:199], v[38:41]
	v_mfma_f32_16x16x32_bf16 v[30:33], v[156:159], v[204:207], v[30:33]
	v_mfma_f32_16x16x32_bf16 v[22:25], v[164:167], v[204:207], v[22:25]
	v_mfma_f32_16x16x32_bf16 v[14:17], v[156:159], v[212:215], v[14:17]
	v_mfma_f32_16x16x32_bf16 v[6:9], v[164:167], v[212:215], v[6:9]
	v_mfma_f32_16x16x32_bf16 v[58:61], v[168:171], v[184:187], v[58:61]
	v_mfma_f32_16x16x32_bf16 v[50:53], v[176:179], v[184:187], v[50:53]
	v_mfma_f32_16x16x32_bf16 v[42:45], v[168:171], v[192:195], v[42:45]
	v_mfma_f32_16x16x32_bf16 v[34:37], v[176:179], v[192:195], v[34:37]
	v_mfma_f32_16x16x32_bf16 v[26:29], v[168:171], v[200:203], v[26:29]
	v_mfma_f32_16x16x32_bf16 v[18:21], v[176:179], v[200:203], v[18:21]
	v_mfma_f32_16x16x32_bf16 v[10:13], v[168:171], v[208:211], v[10:13]
	v_mfma_f32_16x16x32_bf16 v[2:5], v[176:179], v[208:211], v[2:5]
	v_mfma_f32_16x16x32_bf16 v[58:61], v[172:175], v[188:191], v[58:61]
	v_mfma_f32_16x16x32_bf16 v[50:53], v[180:183], v[188:191], v[50:53]
	v_mfma_f32_16x16x32_bf16 v[42:45], v[172:175], v[196:199], v[42:45]
	v_mfma_f32_16x16x32_bf16 v[34:37], v[180:183], v[196:199], v[34:37]
	v_mfma_f32_16x16x32_bf16 v[26:29], v[172:175], v[204:207], v[26:29]
	v_mfma_f32_16x16x32_bf16 v[18:21], v[180:183], v[204:207], v[18:21]
	v_mfma_f32_16x16x32_bf16 v[10:13], v[172:175], v[212:215], v[10:13]
	v_mfma_f32_16x16x32_bf16 v[2:5], v[180:183], v[212:215], v[2:5]
	s_barrier
	s_cbranch_scc0 .LBB0_783
	s_and_b64 vcc, exec, s[40:41]
	s_cbranch_vccz .LBB0_786
	s_barrier

.LBB0_858:
	ds_read_b128 v[26:29], v185
	ds_read_b128 v[30:33], v185 offset:1024
	ds_read_b128 v[18:21], v185 offset:2048
	ds_read_b128 v[22:25], v185 offset:3072
	ds_read_b128 v[10:13], v186
	ds_read_b128 v[14:17], v186 offset:1024
	ds_read_b128 v[2:5], v186 offset:2048
	ds_read_b128 v[6:9], v186 offset:3072
	s_add_u32 s26, s50, 0xfff50080
	s_addc_u32 s27, s51, -1
	s_cmp_eq_u32 s74, 40
	s_cselect_b32 s53, s5, s27
	s_cselect_b32 s52, s4, s26
	s_cselect_b32 s55, s45, s73
	s_cselect_b32 s54, s44, s72
	v_lshl_add_u64 v[176:177], s[50:51], 0, v[168:169]
	s_add_i32 m0, s59, 0xc000
	ds_read_b128 v[190:193], v187
	ds_read_b128 v[194:197], v187 offset:1024
	ds_read_b128 v[198:201], v187 offset:2048
	ds_read_b128 v[202:205], v187 offset:3072
	ds_read_b128 v[206:209], v187 offset:4096
	ds_read_b128 v[210:213], v187 offset:5120
	ds_read_b128 v[220:223], v187 offset:6144
	ds_read_b128 v[224:227], v187 offset:7168
	global_load_lds_dwordx4 v[176:177], off
	v_lshl_add_u64 v[176:177], s[50:51], 0, v[170:171]
	s_add_i32 m0, s59, 0xe000
	s_nop 0
	global_load_lds_dwordx4 v[176:177], off
	s_waitcnt vmcnt(8)
	s_waitcnt lgkmcnt(0)
	s_barrier
	v_mfma_scale_f32_16x16x128_f8f6f4 v[158:161], v[26:33], v[190:197], v[158:161], v188, v189 op_sel_hi:[0,0,0]
	v_mfma_scale_f32_16x16x128_f8f6f4 v[154:157], v[18:25], v[190:197], v[154:157], v188, v189 op_sel_hi:[0,0,0]
	v_mfma_scale_f32_16x16x128_f8f6f4 v[150:153], v[26:33], v[198:205], v[150:153], v188, v189 op_sel_hi:[0,0,0]
	v_mfma_scale_f32_16x16x128_f8f6f4 v[146:149], v[18:25], v[198:205], v[146:149], v188, v189 op_sel_hi:[0,0,0]
	v_mfma_scale_f32_16x16x128_f8f6f4 v[138:141], v[26:33], v[206:213], v[138:141], v188, v189 op_sel_hi:[0,0,0]
	v_mfma_scale_f32_16x16x128_f8f6f4 v[130:133], v[18:25], v[206:213], v[130:133], v188, v189 op_sel_hi:[0,0,0]
	v_mfma_scale_f32_16x16x128_f8f6f4 v[122:125], v[26:33], v[220:227], v[122:125], v188, v189 op_sel_hi:[0,0,0]
	v_mfma_scale_f32_16x16x128_f8f6f4 v[114:117], v[18:25], v[220:227], v[114:117], v188, v189 op_sel_hi:[0,0,0]
	v_mfma_scale_f32_16x16x128_f8f6f4 v[142:145], v[10:17], v[190:197], v[142:145], v188, v189 op_sel_hi:[0,0,0]
	v_mfma_scale_f32_16x16x128_f8f6f4 v[134:137], v[2:9], v[190:197], v[134:137], v188, v189 op_sel_hi:[0,0,0]
	v_mfma_scale_f32_16x16x128_f8f6f4 v[126:129], v[10:17], v[198:205], v[126:129], v188, v189 op_sel_hi:[0,0,0]
	v_mfma_scale_f32_16x16x128_f8f6f4 v[118:121], v[2:9], v[198:205], v[118:121], v188, v189 op_sel_hi:[0,0,0]
	v_mfma_scale_f32_16x16x128_f8f6f4 v[110:113], v[10:17], v[206:213], v[110:113], v188, v189 op_sel_hi:[0,0,0]
	v_mfma_scale_f32_16x16x128_f8f6f4 v[106:109], v[2:9], v[206:213], v[106:109], v188, v189 op_sel_hi:[0,0,0]
	v_mfma_scale_f32_16x16x128_f8f6f4 v[102:105], v[10:17], v[220:227], v[102:105], v188, v189 op_sel_hi:[0,0,0]
	v_mfma_scale_f32_16x16x128_f8f6f4 v[98:101], v[2:9], v[220:227], v[98:101], v188, v189 op_sel_hi:[0,0,0]
	s_barrier
	s_add_i32 s26, s67, s57
	v_lshl_add_u64 v[176:177], s[54:55], 0, v[162:163]
	s_mov_b32 m0, s26
	ds_read_b128 v[190:193], v187 offset:16384
	ds_read_b128 v[194:197], v187 offset:17408
	ds_read_b128 v[198:201], v187 offset:18432
	ds_read_b128 v[202:205], v187 offset:19456
	ds_read_b128 v[206:209], v187 offset:20480
	ds_read_b128 v[210:213], v187 offset:21504
	ds_read_b128 v[220:223], v187 offset:22528
	ds_read_b128 v[224:227], v187 offset:23552
	global_load_lds_dwordx4 v[176:177], off
	v_lshl_add_u64 v[178:179], v[176:177], 0, s[8:9]
	s_add_i32 m0, s26, 0x2000
	s_add_i32 s26, s68, s57
	global_load_lds_dwordx4 v[178:179], off
	v_lshl_add_u64 v[178:179], v[176:177], 0, s[10:11]
	s_mov_b32 m0, s26
	v_lshl_add_u64 v[180:181], s[52:53], 0, v[166:167]
	global_load_lds_dwordx4 v[178:179], off
	v_lshl_add_u64 v[178:179], v[176:177], 0, s[12:13]
	s_add_i32 m0, s26, 0x2000
	s_nop 0
	global_load_lds_dwordx4 v[178:179], off
	v_lshl_add_u64 v[178:179], s[52:53], 0, v[164:165]
	s_mov_b32 m0, s59
	s_nop 0
	global_load_lds_dwordx4 v[178:179], off
	s_mov_b32 m0, s60
	s_nop 0
	global_load_lds_dwordx4 v[180:181], off
	s_waitcnt vmcnt(8)
	s_waitcnt lgkmcnt(0)
	s_barrier
	v_mfma_scale_f32_16x16x128_f8f6f4 v[94:97], v[26:33], v[190:197], v[94:97], v188, v189 op_sel_hi:[0,0,0]
	v_mfma_scale_f32_16x16x128_f8f6f4 v[90:93], v[18:25], v[190:197], v[90:93], v188, v189 op_sel_hi:[0,0,0]
	v_mfma_scale_f32_16x16x128_f8f6f4 v[86:89], v[26:33], v[198:205], v[86:89], v188, v189 op_sel_hi:[0,0,0]
	v_mfma_scale_f32_16x16x128_f8f6f4 v[78:81], v[18:25], v[198:205], v[78:81], v188, v189 op_sel_hi:[0,0,0]
	v_mfma_scale_f32_16x16x128_f8f6f4 v[70:73], v[26:33], v[206:213], v[70:73], v188, v189 op_sel_hi:[0,0,0]
	v_mfma_scale_f32_16x16x128_f8f6f4 v[62:65], v[18:25], v[206:213], v[62:65], v188, v189 op_sel_hi:[0,0,0]
	v_mfma_scale_f32_16x16x128_f8f6f4 v[54:57], v[26:33], v[220:227], v[54:57], v188, v189 op_sel_hi:[0,0,0]
	v_mfma_scale_f32_16x16x128_f8f6f4 v[46:49], v[18:25], v[220:227], v[46:49], v188, v189 op_sel_hi:[0,0,0]
	v_mfma_scale_f32_16x16x128_f8f6f4 v[82:85], v[10:17], v[190:197], v[82:85], v188, v189 op_sel_hi:[0,0,0]
	v_mfma_scale_f32_16x16x128_f8f6f4 v[74:77], v[2:9], v[190:197], v[74:77], v188, v189 op_sel_hi:[0,0,0]
	v_mfma_scale_f32_16x16x128_f8f6f4 v[66:69], v[10:17], v[198:205], v[66:69], v188, v189 op_sel_hi:[0,0,0]
	v_mfma_scale_f32_16x16x128_f8f6f4 v[58:61], v[2:9], v[198:205], v[58:61], v188, v189 op_sel_hi:[0,0,0]
	v_mfma_scale_f32_16x16x128_f8f6f4 v[50:53], v[10:17], v[206:213], v[50:53], v188, v189 op_sel_hi:[0,0,0]
	v_mfma_scale_f32_16x16x128_f8f6f4 v[42:45], v[2:9], v[206:213], v[42:45], v188, v189 op_sel_hi:[0,0,0]
	v_mfma_scale_f32_16x16x128_f8f6f4 v[38:41], v[10:17], v[220:227], v[38:41], v188, v189 op_sel_hi:[0,0,0]
	v_mfma_scale_f32_16x16x128_f8f6f4 v[34:37], v[2:9], v[220:227], v[34:37], v188, v189 op_sel_hi:[0,0,0]
	s_barrier
	s_add_i32 s54, 0, 0x18000
	s_add_i32 s55, 0, 0x1c000
	v_add_u32_e32 v14, s54, v183
	v_add_u32_e32 v30, s55, v183
	ds_read_b128 v[2:5], v14
	ds_read_b128 v[6:9], v14 offset:1024
	ds_read_b128 v[10:13], v14 offset:2048
	ds_read_b128 v[14:17], v14 offset:3072
	ds_read_b128 v[18:21], v30
	ds_read_b128 v[22:25], v30 offset:1024
	ds_read_b128 v[26:29], v30 offset:2048
	ds_read_b128 v[30:33], v30 offset:3072
	s_add_u32 s26, s52, 0xb0000
	s_addc_u32 s27, s53, 0
	s_mov_b32 m0, s61
	v_lshl_add_u64 v[214:215], s[26:27], 0, v[164:165]
	ds_read_b128 v[190:193], v187 offset:32768
	ds_read_b128 v[194:197], v187 offset:33792
	ds_read_b128 v[198:201], v187 offset:34816
	ds_read_b128 v[202:205], v187 offset:35840
	ds_read_b128 v[206:209], v187 offset:36864
	ds_read_b128 v[210:213], v187 offset:37888
	ds_read_b128 v[220:223], v187 offset:38912
	ds_read_b128 v[224:227], v187 offset:39936
	global_load_lds_dwordx4 v[214:215], off
	v_lshl_add_u64 v[214:215], s[26:27], 0, v[166:167]
	s_mov_b32 m0, s62
	s_nop 0
	global_load_lds_dwordx4 v[214:215], off
	s_waitcnt vmcnt(8)
	s_waitcnt lgkmcnt(0)
	s_barrier
	v_mfma_scale_f32_16x16x128_f8f6f4 v[158:161], v[2:9], v[190:197], v[158:161], v188, v189 op_sel_hi:[0,0,0]
	v_mfma_scale_f32_16x16x128_f8f6f4 v[154:157], v[10:17], v[190:197], v[154:157], v188, v189 op_sel_hi:[0,0,0]
	v_mfma_scale_f32_16x16x128_f8f6f4 v[150:153], v[2:9], v[198:205], v[150:153], v188, v189 op_sel_hi:[0,0,0]
	v_mfma_scale_f32_16x16x128_f8f6f4 v[146:149], v[10:17], v[198:205], v[146:149], v188, v189 op_sel_hi:[0,0,0]
	v_mfma_scale_f32_16x16x128_f8f6f4 v[138:141], v[2:9], v[206:213], v[138:141], v188, v189 op_sel_hi:[0,0,0]
	v_mfma_scale_f32_16x16x128_f8f6f4 v[130:133], v[10:17], v[206:213], v[130:133], v188, v189 op_sel_hi:[0,0,0]
	v_mfma_scale_f32_16x16x128_f8f6f4 v[122:125], v[2:9], v[220:227], v[122:125], v188, v189 op_sel_hi:[0,0,0]
	v_mfma_scale_f32_16x16x128_f8f6f4 v[114:117], v[10:17], v[220:227], v[114:117], v188, v189 op_sel_hi:[0,0,0]
	v_mfma_scale_f32_16x16x128_f8f6f4 v[142:145], v[18:25], v[190:197], v[142:145], v188, v189 op_sel_hi:[0,0,0]
	v_mfma_scale_f32_16x16x128_f8f6f4 v[134:137], v[26:33], v[190:197], v[134:137], v188, v189 op_sel_hi:[0,0,0]
	v_mfma_scale_f32_16x16x128_f8f6f4 v[126:129], v[18:25], v[198:205], v[126:129], v188, v189 op_sel_hi:[0,0,0]
	v_mfma_scale_f32_16x16x128_f8f6f4 v[118:121], v[26:33], v[198:205], v[118:121], v188, v189 op_sel_hi:[0,0,0]
	v_mfma_scale_f32_16x16x128_f8f6f4 v[110:113], v[18:25], v[206:213], v[110:113], v188, v189 op_sel_hi:[0,0,0]
	v_mfma_scale_f32_16x16x128_f8f6f4 v[106:109], v[26:33], v[206:213], v[106:109], v188, v189 op_sel_hi:[0,0,0]
	v_mfma_scale_f32_16x16x128_f8f6f4 v[102:105], v[18:25], v[220:227], v[102:105], v188, v189 op_sel_hi:[0,0,0]
	v_mfma_scale_f32_16x16x128_f8f6f4 v[98:101], v[26:33], v[220:227], v[98:101], v188, v189 op_sel_hi:[0,0,0]
	s_barrier
	s_add_i32 s26, s54, s57
	v_lshl_add_u64 v[214:215], v[176:177], 0, s[16:17]
	s_mov_b32 m0, s26
	ds_read_b128 v[190:193], v187 offset:49152
	ds_read_b128 v[194:197], v187 offset:50176
	ds_read_b128 v[198:201], v187 offset:51200
	ds_read_b128 v[202:205], v187 offset:52224
	ds_read_b128 v[206:209], v187 offset:53248
	ds_read_b128 v[210:213], v187 offset:54272
	ds_read_b128 v[220:223], v187 offset:55296
	ds_read_b128 v[224:227], v187 offset:56320
	global_load_lds_dwordx4 v[214:215], off
	v_lshl_add_u64 v[214:215], v[176:177], 0, s[18:19]
	s_add_i32 m0, s26, 0x2000
	s_add_i32 s26, s55, s57
	global_load_lds_dwordx4 v[214:215], off
	v_lshl_add_u64 v[214:215], v[176:177], 0, s[22:23]
	s_mov_b32 m0, s26
	v_lshl_add_u64 v[176:177], v[176:177], 0, s[24:25]
	global_load_lds_dwordx4 v[214:215], off
	s_add_i32 m0, s26, 0x2000
	s_nop 0
	global_load_lds_dwordx4 v[176:177], off
	v_lshl_add_u64 v[176:177], v[178:179], 0, s[20:21]
	s_mov_b32 m0, s64
	s_nop 0
	global_load_lds_dwordx4 v[176:177], off
	v_lshl_add_u64 v[176:177], v[180:181], 0, s[20:21]
	s_mov_b32 m0, s65
	s_nop 0
	global_load_lds_dwordx4 v[176:177], off
	s_waitcnt vmcnt(8)
	s_waitcnt lgkmcnt(0)
	s_barrier
	v_mfma_scale_f32_16x16x128_f8f6f4 v[94:97], v[2:9], v[190:197], v[94:97], v188, v189 op_sel_hi:[0,0,0]
	s_add_i32 s74, s74, 2
	s_add_u32 s72, s72, 0x10000
	s_addc_u32 s73, s73, 0
	s_add_u32 s50, s50, 0x100
	s_addc_u32 s51, s51, 0
	s_cmp_gt_u32 s74, 41
	v_mfma_scale_f32_16x16x128_f8f6f4 v[90:93], v[10:17], v[190:197], v[90:93], v188, v189 op_sel_hi:[0,0,0]
	v_mfma_scale_f32_16x16x128_f8f6f4 v[86:89], v[2:9], v[198:205], v[86:89], v188, v189 op_sel_hi:[0,0,0]
	v_mfma_scale_f32_16x16x128_f8f6f4 v[78:81], v[10:17], v[198:205], v[78:81], v188, v189 op_sel_hi:[0,0,0]
	v_mfma_scale_f32_16x16x128_f8f6f4 v[70:73], v[2:9], v[206:213], v[70:73], v188, v189 op_sel_hi:[0,0,0]
	v_mfma_scale_f32_16x16x128_f8f6f4 v[62:65], v[10:17], v[206:213], v[62:65], v188, v189 op_sel_hi:[0,0,0]
	v_mfma_scale_f32_16x16x128_f8f6f4 v[54:57], v[2:9], v[220:227], v[54:57], v188, v189 op_sel_hi:[0,0,0]
	v_mfma_scale_f32_16x16x128_f8f6f4 v[46:49], v[10:17], v[220:227], v[46:49], v188, v189 op_sel_hi:[0,0,0]
	v_mfma_scale_f32_16x16x128_f8f6f4 v[82:85], v[18:25], v[190:197], v[82:85], v188, v189 op_sel_hi:[0,0,0]
	v_mfma_scale_f32_16x16x128_f8f6f4 v[74:77], v[26:33], v[190:197], v[74:77], v188, v189 op_sel_hi:[0,0,0]
	v_mfma_scale_f32_16x16x128_f8f6f4 v[66:69], v[18:25], v[198:205], v[66:69], v188, v189 op_sel_hi:[0,0,0]
	v_mfma_scale_f32_16x16x128_f8f6f4 v[58:61], v[26:33], v[198:205], v[58:61], v188, v189 op_sel_hi:[0,0,0]
	v_mfma_scale_f32_16x16x128_f8f6f4 v[50:53], v[18:25], v[206:213], v[50:53], v188, v189 op_sel_hi:[0,0,0]
	v_mfma_scale_f32_16x16x128_f8f6f4 v[42:45], v[26:33], v[206:213], v[42:45], v188, v189 op_sel_hi:[0,0,0]
	v_mfma_scale_f32_16x16x128_f8f6f4 v[38:41], v[18:25], v[220:227], v[38:41], v188, v189 op_sel_hi:[0,0,0]
	v_mfma_scale_f32_16x16x128_f8f6f4 v[34:37], v[26:33], v[220:227], v[34:37], v188, v189 op_sel_hi:[0,0,0]
	s_barrier
	s_cbranch_scc0 .LBB0_858
	s_and_b64 vcc, exec, s[40:41]
	s_cbranch_vccz .LBB0_861
	s_barrier

.LBB0_985:
	ds_read_b128 v[26:29], v185
	ds_read_b128 v[30:33], v185 offset:1024
	ds_read_b128 v[18:21], v185 offset:2048
	ds_read_b128 v[22:25], v185 offset:3072
	ds_read_b128 v[10:13], v186
	ds_read_b128 v[14:17], v186 offset:1024
	ds_read_b128 v[2:5], v186 offset:2048
	ds_read_b128 v[6:9], v186 offset:3072
	s_add_u32 s26, s56, 0xfffc0080
	s_addc_u32 s27, s57, -1
	s_cmp_eq_u32 s80, 12
	s_cselect_b32 s59, s45, s27
	s_cselect_b32 s58, s72, s26
	s_cselect_b32 s61, s41, s75
	s_cselect_b32 s60, s73, s74
	v_lshl_add_u64 v[176:177], s[56:57], 0, v[168:169]
	s_add_i32 m0, s55, 0xc000
	ds_read_b128 v[192:195], v187
	ds_read_b128 v[196:199], v187 offset:1024
	ds_read_b128 v[200:203], v187 offset:2048
	ds_read_b128 v[204:207], v187 offset:3072
	ds_read_b128 v[208:211], v187 offset:4096
	ds_read_b128 v[212:215], v187 offset:5120
	ds_read_b128 v[220:223], v187 offset:6144
	ds_read_b128 v[224:227], v187 offset:7168
	global_load_lds_dwordx4 v[176:177], off
	v_lshl_add_u64 v[176:177], s[56:57], 0, v[170:171]
	s_add_i32 m0, s55, 0xe000
	s_nop 0
	global_load_lds_dwordx4 v[176:177], off
	s_waitcnt vmcnt(8)
	s_waitcnt lgkmcnt(0)
	s_barrier
	v_mfma_scale_f32_16x16x128_f8f6f4 v[158:161], v[26:33], v[192:199], v[158:161], v188, v189 op_sel_hi:[0,0,0]
	v_mfma_scale_f32_16x16x128_f8f6f4 v[154:157], v[18:25], v[192:199], v[154:157], v188, v189 op_sel_hi:[0,0,0]
	v_mfma_scale_f32_16x16x128_f8f6f4 v[146:149], v[26:33], v[200:207], v[146:149], v188, v189 op_sel_hi:[0,0,0]
	v_mfma_scale_f32_16x16x128_f8f6f4 v[138:141], v[18:25], v[200:207], v[138:141], v188, v189 op_sel_hi:[0,0,0]
	v_mfma_scale_f32_16x16x128_f8f6f4 v[130:133], v[26:33], v[208:215], v[130:133], v188, v189 op_sel_hi:[0,0,0]
	v_mfma_scale_f32_16x16x128_f8f6f4 v[122:125], v[18:25], v[208:215], v[122:125], v188, v189 op_sel_hi:[0,0,0]
	v_mfma_scale_f32_16x16x128_f8f6f4 v[114:117], v[26:33], v[220:227], v[114:117], v188, v189 op_sel_hi:[0,0,0]
	v_mfma_scale_f32_16x16x128_f8f6f4 v[106:109], v[18:25], v[220:227], v[106:109], v188, v189 op_sel_hi:[0,0,0]
	v_mfma_scale_f32_16x16x128_f8f6f4 v[150:153], v[10:17], v[192:199], v[150:153], v188, v189 op_sel_hi:[0,0,0]
	v_mfma_scale_f32_16x16x128_f8f6f4 v[142:145], v[2:9], v[192:199], v[142:145], v188, v189 op_sel_hi:[0,0,0]
	v_mfma_scale_f32_16x16x128_f8f6f4 v[134:137], v[10:17], v[200:207], v[134:137], v188, v189 op_sel_hi:[0,0,0]
	v_mfma_scale_f32_16x16x128_f8f6f4 v[126:129], v[2:9], v[200:207], v[126:129], v188, v189 op_sel_hi:[0,0,0]
	v_mfma_scale_f32_16x16x128_f8f6f4 v[118:121], v[10:17], v[208:215], v[118:121], v188, v189 op_sel_hi:[0,0,0]
	v_mfma_scale_f32_16x16x128_f8f6f4 v[110:113], v[2:9], v[208:215], v[110:113], v188, v189 op_sel_hi:[0,0,0]
	v_mfma_scale_f32_16x16x128_f8f6f4 v[102:105], v[10:17], v[220:227], v[102:105], v188, v189 op_sel_hi:[0,0,0]
	v_mfma_scale_f32_16x16x128_f8f6f4 v[98:101], v[2:9], v[220:227], v[98:101], v188, v189 op_sel_hi:[0,0,0]
	s_barrier
	s_add_i32 s26, s70, s35
	v_lshl_add_u64 v[176:177], s[60:61], 0, v[162:163]
	s_mov_b32 m0, s26
	ds_read_b128 v[192:195], v187 offset:16384
	ds_read_b128 v[196:199], v187 offset:17408
	ds_read_b128 v[200:203], v187 offset:18432
	ds_read_b128 v[204:207], v187 offset:19456
	ds_read_b128 v[208:211], v187 offset:20480
	ds_read_b128 v[212:215], v187 offset:21504
	ds_read_b128 v[220:223], v187 offset:22528
	ds_read_b128 v[224:227], v187 offset:23552
	global_load_lds_dwordx4 v[176:177], off
	v_lshl_add_u64 v[178:179], v[176:177], 0, s[6:7]
	s_add_i32 m0, s26, 0x2000
	s_add_i32 s26, s71, s35
	global_load_lds_dwordx4 v[178:179], off
	v_lshl_add_u64 v[178:179], v[176:177], 0, s[8:9]
	s_mov_b32 m0, s26
	v_lshl_add_u64 v[180:181], s[58:59], 0, v[166:167]
	global_load_lds_dwordx4 v[178:179], off
	v_lshl_add_u64 v[178:179], v[176:177], 0, s[10:11]
	s_add_i32 m0, s26, 0x2000
	s_nop 0
	global_load_lds_dwordx4 v[178:179], off
	v_lshl_add_u64 v[178:179], s[58:59], 0, v[164:165]
	s_mov_b32 m0, s55
	s_nop 0
	global_load_lds_dwordx4 v[178:179], off
	s_mov_b32 m0, s63
	s_nop 0
	global_load_lds_dwordx4 v[180:181], off
	s_waitcnt vmcnt(8)
	s_waitcnt lgkmcnt(0)
	s_barrier
	v_mfma_scale_f32_16x16x128_f8f6f4 v[94:97], v[26:33], v[192:199], v[94:97], v188, v189 op_sel_hi:[0,0,0]
	v_mfma_scale_f32_16x16x128_f8f6f4 v[90:93], v[18:25], v[192:199], v[90:93], v188, v189 op_sel_hi:[0,0,0]
	v_mfma_scale_f32_16x16x128_f8f6f4 v[82:85], v[26:33], v[200:207], v[82:85], v188, v189 op_sel_hi:[0,0,0]
	v_mfma_scale_f32_16x16x128_f8f6f4 v[74:77], v[18:25], v[200:207], v[74:77], v188, v189 op_sel_hi:[0,0,0]
	v_mfma_scale_f32_16x16x128_f8f6f4 v[66:69], v[26:33], v[208:215], v[66:69], v188, v189 op_sel_hi:[0,0,0]
	v_mfma_scale_f32_16x16x128_f8f6f4 v[58:61], v[18:25], v[208:215], v[58:61], v188, v189 op_sel_hi:[0,0,0]
	v_mfma_scale_f32_16x16x128_f8f6f4 v[50:53], v[26:33], v[220:227], v[50:53], v188, v189 op_sel_hi:[0,0,0]
	v_mfma_scale_f32_16x16x128_f8f6f4 v[42:45], v[18:25], v[220:227], v[42:45], v188, v189 op_sel_hi:[0,0,0]
	v_mfma_scale_f32_16x16x128_f8f6f4 v[86:89], v[10:17], v[192:199], v[86:89], v188, v189 op_sel_hi:[0,0,0]
	v_mfma_scale_f32_16x16x128_f8f6f4 v[78:81], v[2:9], v[192:199], v[78:81], v188, v189 op_sel_hi:[0,0,0]
	v_mfma_scale_f32_16x16x128_f8f6f4 v[70:73], v[10:17], v[200:207], v[70:73], v188, v189 op_sel_hi:[0,0,0]
	v_mfma_scale_f32_16x16x128_f8f6f4 v[62:65], v[2:9], v[200:207], v[62:65], v188, v189 op_sel_hi:[0,0,0]
	v_mfma_scale_f32_16x16x128_f8f6f4 v[54:57], v[10:17], v[208:215], v[54:57], v188, v189 op_sel_hi:[0,0,0]
	v_mfma_scale_f32_16x16x128_f8f6f4 v[46:49], v[2:9], v[208:215], v[46:49], v188, v189 op_sel_hi:[0,0,0]
	v_mfma_scale_f32_16x16x128_f8f6f4 v[38:41], v[10:17], v[220:227], v[38:41], v188, v189 op_sel_hi:[0,0,0]
	v_mfma_scale_f32_16x16x128_f8f6f4 v[34:37], v[2:9], v[220:227], v[34:37], v188, v189 op_sel_hi:[0,0,0]
	s_barrier
	s_add_i32 s60, 0, 0x18000
	s_add_i32 s61, 0, 0x1c000
	v_add_u32_e32 v14, s60, v183
	v_add_u32_e32 v30, s61, v183
	ds_read_b128 v[2:5], v14
	ds_read_b128 v[6:9], v14 offset:1024
	ds_read_b128 v[10:13], v14 offset:2048
	ds_read_b128 v[14:17], v14 offset:3072
	ds_read_b128 v[18:21], v30
	ds_read_b128 v[22:25], v30 offset:1024
	ds_read_b128 v[26:29], v30 offset:2048
	ds_read_b128 v[30:33], v30 offset:3072
	s_add_u32 s26, s58, 0x40000
	s_addc_u32 s27, s59, 0
	s_mov_b32 m0, s64
	v_lshl_add_u64 v[216:217], s[26:27], 0, v[164:165]
	ds_read_b128 v[192:195], v187 offset:32768
	ds_read_b128 v[196:199], v187 offset:33792
	ds_read_b128 v[200:203], v187 offset:34816
	ds_read_b128 v[204:207], v187 offset:35840
	ds_read_b128 v[208:211], v187 offset:36864
	ds_read_b128 v[212:215], v187 offset:37888
	ds_read_b128 v[220:223], v187 offset:38912
	ds_read_b128 v[224:227], v187 offset:39936
	global_load_lds_dwordx4 v[216:217], off
	v_lshl_add_u64 v[216:217], s[26:27], 0, v[166:167]
	s_mov_b32 m0, s65
	s_nop 0
	global_load_lds_dwordx4 v[216:217], off
	s_waitcnt vmcnt(8)
	s_waitcnt lgkmcnt(0)
	s_barrier
	v_mfma_scale_f32_16x16x128_f8f6f4 v[158:161], v[2:9], v[192:199], v[158:161], v188, v189 op_sel_hi:[0,0,0]
	v_mfma_scale_f32_16x16x128_f8f6f4 v[154:157], v[10:17], v[192:199], v[154:157], v188, v189 op_sel_hi:[0,0,0]
	v_mfma_scale_f32_16x16x128_f8f6f4 v[146:149], v[2:9], v[200:207], v[146:149], v188, v189 op_sel_hi:[0,0,0]
	v_mfma_scale_f32_16x16x128_f8f6f4 v[138:141], v[10:17], v[200:207], v[138:141], v188, v189 op_sel_hi:[0,0,0]
	v_mfma_scale_f32_16x16x128_f8f6f4 v[130:133], v[2:9], v[208:215], v[130:133], v188, v189 op_sel_hi:[0,0,0]
	v_mfma_scale_f32_16x16x128_f8f6f4 v[122:125], v[10:17], v[208:215], v[122:125], v188, v189 op_sel_hi:[0,0,0]
	v_mfma_scale_f32_16x16x128_f8f6f4 v[114:117], v[2:9], v[220:227], v[114:117], v188, v189 op_sel_hi:[0,0,0]
	v_mfma_scale_f32_16x16x128_f8f6f4 v[106:109], v[10:17], v[220:227], v[106:109], v188, v189 op_sel_hi:[0,0,0]
	v_mfma_scale_f32_16x16x128_f8f6f4 v[150:153], v[18:25], v[192:199], v[150:153], v188, v189 op_sel_hi:[0,0,0]
	v_mfma_scale_f32_16x16x128_f8f6f4 v[142:145], v[26:33], v[192:199], v[142:145], v188, v189 op_sel_hi:[0,0,0]
	v_mfma_scale_f32_16x16x128_f8f6f4 v[134:137], v[18:25], v[200:207], v[134:137], v188, v189 op_sel_hi:[0,0,0]
	v_mfma_scale_f32_16x16x128_f8f6f4 v[126:129], v[26:33], v[200:207], v[126:129], v188, v189 op_sel_hi:[0,0,0]
	v_mfma_scale_f32_16x16x128_f8f6f4 v[118:121], v[18:25], v[208:215], v[118:121], v188, v189 op_sel_hi:[0,0,0]
	v_mfma_scale_f32_16x16x128_f8f6f4 v[110:113], v[26:33], v[208:215], v[110:113], v188, v189 op_sel_hi:[0,0,0]
	v_mfma_scale_f32_16x16x128_f8f6f4 v[102:105], v[18:25], v[220:227], v[102:105], v188, v189 op_sel_hi:[0,0,0]
	v_mfma_scale_f32_16x16x128_f8f6f4 v[98:101], v[26:33], v[220:227], v[98:101], v188, v189 op_sel_hi:[0,0,0]
	s_barrier
	s_add_i32 s26, s60, s35
	v_lshl_add_u64 v[216:217], v[176:177], 0, s[14:15]
	s_mov_b32 m0, s26
	ds_read_b128 v[192:195], v187 offset:49152
	ds_read_b128 v[196:199], v187 offset:50176
	ds_read_b128 v[200:203], v187 offset:51200
	ds_read_b128 v[204:207], v187 offset:52224
	ds_read_b128 v[208:211], v187 offset:53248
	ds_read_b128 v[212:215], v187 offset:54272
	ds_read_b128 v[220:223], v187 offset:55296
	ds_read_b128 v[224:227], v187 offset:56320
	global_load_lds_dwordx4 v[216:217], off
	v_lshl_add_u64 v[216:217], v[176:177], 0, s[16:17]
	s_add_i32 m0, s26, 0x2000
	s_add_i32 s26, s61, s35
	global_load_lds_dwordx4 v[216:217], off
	v_lshl_add_u64 v[216:217], v[176:177], 0, s[20:21]
	s_mov_b32 m0, s26
	v_lshl_add_u64 v[176:177], v[176:177], 0, s[22:23]
	global_load_lds_dwordx4 v[216:217], off
	s_add_i32 m0, s26, 0x2000
	s_nop 0
	global_load_lds_dwordx4 v[176:177], off
	v_lshl_add_u64 v[176:177], v[178:179], 0, s[18:19]
	s_mov_b32 m0, s67
	s_nop 0
	global_load_lds_dwordx4 v[176:177], off
	v_lshl_add_u64 v[176:177], v[180:181], 0, s[18:19]
	s_mov_b32 m0, s68
	s_nop 0
	global_load_lds_dwordx4 v[176:177], off
	s_waitcnt vmcnt(8)
	s_waitcnt lgkmcnt(0)
	s_barrier
	v_mfma_scale_f32_16x16x128_f8f6f4 v[94:97], v[2:9], v[192:199], v[94:97], v188, v189 op_sel_hi:[0,0,0]
	s_add_i32 s80, s80, 2
	s_add_u32 s74, s74, 0x10000
	s_addc_u32 s75, s75, 0
	s_add_u32 s56, s56, 0x100
	s_addc_u32 s57, s57, 0
	s_cmp_gt_u32 s80, 13
	v_mfma_scale_f32_16x16x128_f8f6f4 v[90:93], v[10:17], v[192:199], v[90:93], v188, v189 op_sel_hi:[0,0,0]
	v_mfma_scale_f32_16x16x128_f8f6f4 v[82:85], v[2:9], v[200:207], v[82:85], v188, v189 op_sel_hi:[0,0,0]
	v_mfma_scale_f32_16x16x128_f8f6f4 v[74:77], v[10:17], v[200:207], v[74:77], v188, v189 op_sel_hi:[0,0,0]
	v_mfma_scale_f32_16x16x128_f8f6f4 v[66:69], v[2:9], v[208:215], v[66:69], v188, v189 op_sel_hi:[0,0,0]
	v_mfma_scale_f32_16x16x128_f8f6f4 v[58:61], v[10:17], v[208:215], v[58:61], v188, v189 op_sel_hi:[0,0,0]
	v_mfma_scale_f32_16x16x128_f8f6f4 v[50:53], v[2:9], v[220:227], v[50:53], v188, v189 op_sel_hi:[0,0,0]
	v_mfma_scale_f32_16x16x128_f8f6f4 v[42:45], v[10:17], v[220:227], v[42:45], v188, v189 op_sel_hi:[0,0,0]
	v_mfma_scale_f32_16x16x128_f8f6f4 v[86:89], v[18:25], v[192:199], v[86:89], v188, v189 op_sel_hi:[0,0,0]
	v_mfma_scale_f32_16x16x128_f8f6f4 v[78:81], v[26:33], v[192:199], v[78:81], v188, v189 op_sel_hi:[0,0,0]
	v_mfma_scale_f32_16x16x128_f8f6f4 v[70:73], v[18:25], v[200:207], v[70:73], v188, v189 op_sel_hi:[0,0,0]
	v_mfma_scale_f32_16x16x128_f8f6f4 v[62:65], v[26:33], v[200:207], v[62:65], v188, v189 op_sel_hi:[0,0,0]
	v_mfma_scale_f32_16x16x128_f8f6f4 v[54:57], v[18:25], v[208:215], v[54:57], v188, v189 op_sel_hi:[0,0,0]
	v_mfma_scale_f32_16x16x128_f8f6f4 v[46:49], v[26:33], v[208:215], v[46:49], v188, v189 op_sel_hi:[0,0,0]
	v_mfma_scale_f32_16x16x128_f8f6f4 v[38:41], v[18:25], v[220:227], v[38:41], v188, v189 op_sel_hi:[0,0,0]
	v_mfma_scale_f32_16x16x128_f8f6f4 v[34:37], v[26:33], v[220:227], v[34:37], v188, v189 op_sel_hi:[0,0,0]
	s_barrier
	s_cbranch_scc0 .LBB0_985
	s_and_b64 vcc, exec, s[24:25]
	s_cbranch_vccz .LBB0_988
	s_barrier

.LBB0_1192:
	ds_read_b128 v[66:69], v199
	ds_read_b128 v[70:73], v199 offset:1024
	ds_read_b128 v[82:85], v199 offset:2048
	ds_read_b128 v[86:89], v199 offset:3072
	ds_read_b128 v[146:149], v200
	ds_read_b128 v[150:153], v200 offset:1024
	ds_read_b128 v[154:157], v200 offset:2048
	ds_read_b128 v[158:161], v200 offset:3072
	s_add_u32 s26, s56, 0xfffc0080
	s_addc_u32 s27, s57, -1
	s_cmp_eq_u32 s73, 12
	s_cselect_b32 s59, s45, s27
	s_cselect_b32 s58, s69, s26
	s_cselect_b32 s27, s41, s72
	s_cselect_b32 s26, s70, s71
	v_lshl_add_u64 v[214:215], s[56:57], 0, v[176:177]
	s_add_i32 m0, s55, 0xc000
	ds_read_b128 v[162:165], v201
	ds_read_b128 v[166:169], v201 offset:1024
	ds_read_b128 v[184:187], v201 offset:2048
	ds_read_b128 v[188:191], v201 offset:3072
	ds_read_b128 v[192:195], v201 offset:4096
	ds_read_b128 v[202:205], v201 offset:5120
	ds_read_b128 v[206:209], v201 offset:6144
	ds_read_b128 v[210:213], v201 offset:7168
	global_load_lds_dwordx4 v[214:215], off
	v_lshl_add_u64 v[214:215], s[56:57], 0, v[178:179]
	s_add_i32 m0, s55, 0xe000
	s_nop 0
	global_load_lds_dwordx4 v[214:215], off
	s_waitcnt vmcnt(8)
	s_waitcnt lgkmcnt(0)
	s_barrier
	v_mfma_f32_16x16x32_bf16 v[142:145], v[66:69], v[162:165], v[142:145]
	v_mfma_f32_16x16x32_bf16 v[138:141], v[82:85], v[162:165], v[138:141]
	v_mfma_f32_16x16x32_bf16 v[126:129], v[66:69], v[184:187], v[126:129]
	v_mfma_f32_16x16x32_bf16 v[122:125], v[82:85], v[184:187], v[122:125]
	v_mfma_f32_16x16x32_bf16 v[110:113], v[66:69], v[192:195], v[110:113]
	v_mfma_f32_16x16x32_bf16 v[106:109], v[82:85], v[192:195], v[106:109]
	v_mfma_f32_16x16x32_bf16 v[94:97], v[66:69], v[206:209], v[94:97]
	v_mfma_f32_16x16x32_bf16 v[90:93], v[82:85], v[206:209], v[90:93]
	v_mfma_f32_16x16x32_bf16 v[142:145], v[70:73], v[166:169], v[142:145]
	v_mfma_f32_16x16x32_bf16 v[138:141], v[86:89], v[166:169], v[138:141]
	v_mfma_f32_16x16x32_bf16 v[126:129], v[70:73], v[188:191], v[126:129]
	v_mfma_f32_16x16x32_bf16 v[122:125], v[86:89], v[188:191], v[122:125]
	v_mfma_f32_16x16x32_bf16 v[110:113], v[70:73], v[202:205], v[110:113]
	v_mfma_f32_16x16x32_bf16 v[106:109], v[86:89], v[202:205], v[106:109]
	v_mfma_f32_16x16x32_bf16 v[94:97], v[70:73], v[210:213], v[94:97]
	v_mfma_f32_16x16x32_bf16 v[90:93], v[86:89], v[210:213], v[90:93]
	v_mfma_f32_16x16x32_bf16 v[134:137], v[146:149], v[162:165], v[134:137]
	v_mfma_f32_16x16x32_bf16 v[130:133], v[154:157], v[162:165], v[130:133]
	v_mfma_f32_16x16x32_bf16 v[118:121], v[146:149], v[184:187], v[118:121]
	v_mfma_f32_16x16x32_bf16 v[114:117], v[154:157], v[184:187], v[114:117]
	v_mfma_f32_16x16x32_bf16 v[102:105], v[146:149], v[192:195], v[102:105]
	v_mfma_f32_16x16x32_bf16 v[98:101], v[154:157], v[192:195], v[98:101]
	v_mfma_f32_16x16x32_bf16 v[78:81], v[146:149], v[206:209], v[78:81]
	v_mfma_f32_16x16x32_bf16 v[74:77], v[154:157], v[206:209], v[74:77]
	v_mfma_f32_16x16x32_bf16 v[134:137], v[150:153], v[166:169], v[134:137]
	v_mfma_f32_16x16x32_bf16 v[130:133], v[158:161], v[166:169], v[130:133]
	v_mfma_f32_16x16x32_bf16 v[118:121], v[150:153], v[188:191], v[118:121]
	v_mfma_f32_16x16x32_bf16 v[114:117], v[158:161], v[188:191], v[114:117]
	v_mfma_f32_16x16x32_bf16 v[102:105], v[150:153], v[202:205], v[102:105]
	v_mfma_f32_16x16x32_bf16 v[98:101], v[158:161], v[202:205], v[98:101]
	v_mfma_f32_16x16x32_bf16 v[78:81], v[150:153], v[210:213], v[78:81]
	v_mfma_f32_16x16x32_bf16 v[74:77], v[158:161], v[210:213], v[74:77]
	s_barrier
	v_lshl_add_u64 v[214:215], s[26:27], 0, v[170:171]
	s_add_i32 s26, s67, s35
	s_mov_b32 m0, s26
	ds_read_b128 v[162:165], v201 offset:16384
	ds_read_b128 v[166:169], v201 offset:17408
	ds_read_b128 v[184:187], v201 offset:18432
	ds_read_b128 v[188:191], v201 offset:19456
	ds_read_b128 v[192:195], v201 offset:20480
	ds_read_b128 v[202:205], v201 offset:21504
	ds_read_b128 v[206:209], v201 offset:22528
	ds_read_b128 v[210:213], v201 offset:23552
	global_load_lds_dwordx4 v[214:215], off
	v_lshl_add_u64 v[216:217], v[214:215], 0, s[6:7]
	s_add_i32 m0, s26, 0x2000
	s_add_i32 s26, s68, s35
	global_load_lds_dwordx4 v[216:217], off
	v_lshl_add_u64 v[216:217], v[214:215], 0, s[10:11]
	s_mov_b32 m0, s26
	v_lshl_add_u64 v[220:221], s[58:59], 0, v[174:175]
	global_load_lds_dwordx4 v[216:217], off
	v_lshl_add_u64 v[216:217], v[214:215], 0, s[12:13]
	s_add_i32 m0, s26, 0x2000
	s_nop 0
	global_load_lds_dwordx4 v[216:217], off
	v_lshl_add_u64 v[216:217], s[58:59], 0, v[172:173]
	s_mov_b32 m0, s55
	s_nop 0
	global_load_lds_dwordx4 v[216:217], off
	s_mov_b32 m0, s60
	s_nop 0
	global_load_lds_dwordx4 v[220:221], off
	s_waitcnt vmcnt(8)
	s_waitcnt lgkmcnt(0)
	s_barrier
	v_mfma_f32_16x16x32_bf16 v[62:65], v[66:69], v[162:165], v[62:65]
	v_mfma_f32_16x16x32_bf16 v[58:61], v[82:85], v[162:165], v[58:61]
	v_mfma_f32_16x16x32_bf16 v[46:49], v[66:69], v[184:187], v[46:49]
	v_mfma_f32_16x16x32_bf16 v[42:45], v[82:85], v[184:187], v[42:45]
	v_mfma_f32_16x16x32_bf16 v[30:33], v[66:69], v[192:195], v[30:33]
	v_mfma_f32_16x16x32_bf16 v[26:29], v[82:85], v[192:195], v[26:29]
	v_mfma_f32_16x16x32_bf16 v[14:17], v[66:69], v[206:209], v[14:17]
	v_mfma_f32_16x16x32_bf16 v[10:13], v[82:85], v[206:209], v[10:13]
	v_mfma_f32_16x16x32_bf16 v[62:65], v[70:73], v[166:169], v[62:65]
	v_mfma_f32_16x16x32_bf16 v[58:61], v[86:89], v[166:169], v[58:61]
	v_mfma_f32_16x16x32_bf16 v[46:49], v[70:73], v[188:191], v[46:49]
	v_mfma_f32_16x16x32_bf16 v[42:45], v[86:89], v[188:191], v[42:45]
	v_mfma_f32_16x16x32_bf16 v[30:33], v[70:73], v[202:205], v[30:33]
	v_mfma_f32_16x16x32_bf16 v[26:29], v[86:89], v[202:205], v[26:29]
	v_mfma_f32_16x16x32_bf16 v[14:17], v[70:73], v[210:213], v[14:17]
	v_mfma_f32_16x16x32_bf16 v[10:13], v[86:89], v[210:213], v[10:13]
	v_mfma_f32_16x16x32_bf16 v[54:57], v[146:149], v[162:165], v[54:57]
	v_mfma_f32_16x16x32_bf16 v[50:53], v[154:157], v[162:165], v[50:53]
	v_mfma_f32_16x16x32_bf16 v[38:41], v[146:149], v[184:187], v[38:41]
	v_mfma_f32_16x16x32_bf16 v[34:37], v[154:157], v[184:187], v[34:37]
	v_mfma_f32_16x16x32_bf16 v[22:25], v[146:149], v[192:195], v[22:25]
	v_mfma_f32_16x16x32_bf16 v[18:21], v[154:157], v[192:195], v[18:21]
	v_mfma_f32_16x16x32_bf16 v[6:9], v[146:149], v[206:209], v[6:9]
	v_mfma_f32_16x16x32_bf16 v[2:5], v[154:157], v[206:209], v[2:5]
	v_mfma_f32_16x16x32_bf16 v[54:57], v[150:153], v[166:169], v[54:57]
	v_mfma_f32_16x16x32_bf16 v[50:53], v[158:161], v[166:169], v[50:53]
	v_mfma_f32_16x16x32_bf16 v[38:41], v[150:153], v[188:191], v[38:41]
	v_mfma_f32_16x16x32_bf16 v[34:37], v[158:161], v[188:191], v[34:37]
	v_mfma_f32_16x16x32_bf16 v[22:25], v[150:153], v[202:205], v[22:25]
	v_mfma_f32_16x16x32_bf16 v[18:21], v[158:161], v[202:205], v[18:21]
	v_mfma_f32_16x16x32_bf16 v[6:9], v[150:153], v[210:213], v[6:9]
	v_mfma_f32_16x16x32_bf16 v[2:5], v[158:161], v[210:213], v[2:5]
	s_barrier
	s_add_i32 s74, 0, 0x18000
	s_add_i32 s75, 0, 0x1c000
	v_add_u32_e32 v86, s74, v197
	v_add_u32_e32 v158, s75, v197
	ds_read_b128 v[66:69], v86
	ds_read_b128 v[70:73], v86 offset:1024
	ds_read_b128 v[82:85], v86 offset:2048
	ds_read_b128 v[86:89], v86 offset:3072
	ds_read_b128 v[146:149], v158
	ds_read_b128 v[150:153], v158 offset:1024
	ds_read_b128 v[154:157], v158 offset:2048
	ds_read_b128 v[158:161], v158 offset:3072
	s_add_u32 s26, s58, 0x40000
	s_addc_u32 s27, s59, 0
	s_mov_b32 m0, s61
	v_lshl_add_u64 v[222:223], s[26:27], 0, v[172:173]
	ds_read_b128 v[162:165], v201 offset:32768
	ds_read_b128 v[166:169], v201 offset:33792
	ds_read_b128 v[184:187], v201 offset:34816
	ds_read_b128 v[188:191], v201 offset:35840
	ds_read_b128 v[192:195], v201 offset:36864
	ds_read_b128 v[202:205], v201 offset:37888
	ds_read_b128 v[206:209], v201 offset:38912
	ds_read_b128 v[210:213], v201 offset:39936
	global_load_lds_dwordx4 v[222:223], off
	v_lshl_add_u64 v[222:223], s[26:27], 0, v[174:175]
	s_mov_b32 m0, s62
	s_nop 0
	global_load_lds_dwordx4 v[222:223], off
	s_waitcnt vmcnt(8)
	s_waitcnt lgkmcnt(0)
	s_barrier
	v_mfma_f32_16x16x32_bf16 v[142:145], v[66:69], v[162:165], v[142:145]
	v_mfma_f32_16x16x32_bf16 v[138:141], v[82:85], v[162:165], v[138:141]
	v_mfma_f32_16x16x32_bf16 v[126:129], v[66:69], v[184:187], v[126:129]
	v_mfma_f32_16x16x32_bf16 v[122:125], v[82:85], v[184:187], v[122:125]
	v_mfma_f32_16x16x32_bf16 v[110:113], v[66:69], v[192:195], v[110:113]
	v_mfma_f32_16x16x32_bf16 v[106:109], v[82:85], v[192:195], v[106:109]
	v_mfma_f32_16x16x32_bf16 v[94:97], v[66:69], v[206:209], v[94:97]
	v_mfma_f32_16x16x32_bf16 v[90:93], v[82:85], v[206:209], v[90:93]
	v_mfma_f32_16x16x32_bf16 v[142:145], v[70:73], v[166:169], v[142:145]
	v_mfma_f32_16x16x32_bf16 v[138:141], v[86:89], v[166:169], v[138:141]
	v_mfma_f32_16x16x32_bf16 v[126:129], v[70:73], v[188:191], v[126:129]
	v_mfma_f32_16x16x32_bf16 v[122:125], v[86:89], v[188:191], v[122:125]
	v_mfma_f32_16x16x32_bf16 v[110:113], v[70:73], v[202:205], v[110:113]
	v_mfma_f32_16x16x32_bf16 v[106:109], v[86:89], v[202:205], v[106:109]
	v_mfma_f32_16x16x32_bf16 v[94:97], v[70:73], v[210:213], v[94:97]
	v_mfma_f32_16x16x32_bf16 v[90:93], v[86:89], v[210:213], v[90:93]
	v_mfma_f32_16x16x32_bf16 v[134:137], v[146:149], v[162:165], v[134:137]
	v_mfma_f32_16x16x32_bf16 v[130:133], v[154:157], v[162:165], v[130:133]
	v_mfma_f32_16x16x32_bf16 v[118:121], v[146:149], v[184:187], v[118:121]
	v_mfma_f32_16x16x32_bf16 v[114:117], v[154:157], v[184:187], v[114:117]
	v_mfma_f32_16x16x32_bf16 v[102:105], v[146:149], v[192:195], v[102:105]
	v_mfma_f32_16x16x32_bf16 v[98:101], v[154:157], v[192:195], v[98:101]
	v_mfma_f32_16x16x32_bf16 v[78:81], v[146:149], v[206:209], v[78:81]
	v_mfma_f32_16x16x32_bf16 v[74:77], v[154:157], v[206:209], v[74:77]
	v_mfma_f32_16x16x32_bf16 v[134:137], v[150:153], v[166:169], v[134:137]
	v_mfma_f32_16x16x32_bf16 v[130:133], v[158:161], v[166:169], v[130:133]
	v_mfma_f32_16x16x32_bf16 v[118:121], v[150:153], v[188:191], v[118:121]
	v_mfma_f32_16x16x32_bf16 v[114:117], v[158:161], v[188:191], v[114:117]
	v_mfma_f32_16x16x32_bf16 v[102:105], v[150:153], v[202:205], v[102:105]
	v_mfma_f32_16x16x32_bf16 v[98:101], v[158:161], v[202:205], v[98:101]
	v_mfma_f32_16x16x32_bf16 v[78:81], v[150:153], v[210:213], v[78:81]
	v_mfma_f32_16x16x32_bf16 v[74:77], v[158:161], v[210:213], v[74:77]
	s_barrier
	s_add_i32 s26, s74, s35
	v_lshl_add_u64 v[222:223], v[214:215], 0, s[16:17]
	s_mov_b32 m0, s26
	ds_read_b128 v[162:165], v201 offset:49152
	ds_read_b128 v[166:169], v201 offset:50176
	ds_read_b128 v[184:187], v201 offset:51200
	ds_read_b128 v[188:191], v201 offset:52224
	ds_read_b128 v[192:195], v201 offset:53248
	ds_read_b128 v[202:205], v201 offset:54272
	ds_read_b128 v[206:209], v201 offset:55296
	ds_read_b128 v[210:213], v201 offset:56320
	global_load_lds_dwordx4 v[222:223], off
	v_lshl_add_u64 v[222:223], v[214:215], 0, s[18:19]
	s_add_i32 m0, s26, 0x2000
	s_add_i32 s26, s75, s35
	global_load_lds_dwordx4 v[222:223], off
	v_lshl_add_u64 v[222:223], v[214:215], 0, s[22:23]
	s_mov_b32 m0, s26
	v_lshl_add_u64 v[214:215], v[214:215], 0, s[24:25]
	global_load_lds_dwordx4 v[222:223], off
	s_add_i32 m0, s26, 0x2000
	s_nop 0
	global_load_lds_dwordx4 v[214:215], off
	v_lshl_add_u64 v[214:215], v[216:217], 0, s[20:21]
	s_mov_b32 m0, s64
	s_nop 0
	global_load_lds_dwordx4 v[214:215], off
	v_lshl_add_u64 v[214:215], v[220:221], 0, s[20:21]
	s_mov_b32 m0, s65
	s_nop 0
	global_load_lds_dwordx4 v[214:215], off
	s_waitcnt vmcnt(8)
	s_waitcnt lgkmcnt(0)
	s_barrier
	v_mfma_f32_16x16x32_bf16 v[62:65], v[66:69], v[162:165], v[62:65]
	s_add_i32 s73, s73, 2
	s_add_u32 s71, s71, 0x10000
	s_addc_u32 s72, s72, 0
	s_add_u32 s56, s56, 0x100
	s_addc_u32 s57, s57, 0
	s_cmp_gt_u32 s73, 13
	v_mfma_f32_16x16x32_bf16 v[58:61], v[82:85], v[162:165], v[58:61]
	v_mfma_f32_16x16x32_bf16 v[46:49], v[66:69], v[184:187], v[46:49]
	v_mfma_f32_16x16x32_bf16 v[42:45], v[82:85], v[184:187], v[42:45]
	v_mfma_f32_16x16x32_bf16 v[30:33], v[66:69], v[192:195], v[30:33]
	v_mfma_f32_16x16x32_bf16 v[26:29], v[82:85], v[192:195], v[26:29]
	v_mfma_f32_16x16x32_bf16 v[14:17], v[66:69], v[206:209], v[14:17]
	v_mfma_f32_16x16x32_bf16 v[10:13], v[82:85], v[206:209], v[10:13]
	v_mfma_f32_16x16x32_bf16 v[62:65], v[70:73], v[166:169], v[62:65]
	v_mfma_f32_16x16x32_bf16 v[58:61], v[86:89], v[166:169], v[58:61]
	v_mfma_f32_16x16x32_bf16 v[46:49], v[70:73], v[188:191], v[46:49]
	v_mfma_f32_16x16x32_bf16 v[42:45], v[86:89], v[188:191], v[42:45]
	v_mfma_f32_16x16x32_bf16 v[30:33], v[70:73], v[202:205], v[30:33]
	v_mfma_f32_16x16x32_bf16 v[26:29], v[86:89], v[202:205], v[26:29]
	v_mfma_f32_16x16x32_bf16 v[14:17], v[70:73], v[210:213], v[14:17]
	v_mfma_f32_16x16x32_bf16 v[10:13], v[86:89], v[210:213], v[10:13]
	v_mfma_f32_16x16x32_bf16 v[54:57], v[146:149], v[162:165], v[54:57]
	v_mfma_f32_16x16x32_bf16 v[50:53], v[154:157], v[162:165], v[50:53]
	v_mfma_f32_16x16x32_bf16 v[38:41], v[146:149], v[184:187], v[38:41]
	v_mfma_f32_16x16x32_bf16 v[34:37], v[154:157], v[184:187], v[34:37]
	v_mfma_f32_16x16x32_bf16 v[22:25], v[146:149], v[192:195], v[22:25]
	v_mfma_f32_16x16x32_bf16 v[18:21], v[154:157], v[192:195], v[18:21]
	v_mfma_f32_16x16x32_bf16 v[6:9], v[146:149], v[206:209], v[6:9]
	v_mfma_f32_16x16x32_bf16 v[2:5], v[154:157], v[206:209], v[2:5]
	v_mfma_f32_16x16x32_bf16 v[54:57], v[150:153], v[166:169], v[54:57]
	v_mfma_f32_16x16x32_bf16 v[50:53], v[158:161], v[166:169], v[50:53]
	v_mfma_f32_16x16x32_bf16 v[38:41], v[150:153], v[188:191], v[38:41]
	v_mfma_f32_16x16x32_bf16 v[34:37], v[158:161], v[188:191], v[34:37]
	v_mfma_f32_16x16x32_bf16 v[22:25], v[150:153], v[202:205], v[22:25]
	v_mfma_f32_16x16x32_bf16 v[18:21], v[158:161], v[202:205], v[18:21]
	v_mfma_f32_16x16x32_bf16 v[6:9], v[150:153], v[210:213], v[6:9]
	v_mfma_f32_16x16x32_bf16 v[2:5], v[158:161], v[210:213], v[2:5]
	s_barrier
	s_cbranch_scc0 .LBB0_1192
	s_and_b64 vcc, exec, s[36:37]
	s_cbranch_vccz .LBB0_1195
	s_barrier

.LBB0_1271:
	ds_read_b128 v[144:147], v158
	ds_read_b128 v[148:151], v158 offset:1024
	ds_read_b128 v[152:155], v158 offset:2048
	ds_read_b128 v[162:165], v158 offset:3072
	ds_read_b128 v[166:169], v159
	ds_read_b128 v[170:173], v159 offset:1024
	ds_read_b128 v[174:177], v159 offset:2048
	ds_read_b128 v[178:181], v159 offset:3072
	s_add_u32 s26, s58, 0xfff80080
	s_addc_u32 s27, s59, -1
	s_cmp_eq_u32 s80, 28
	s_cselect_b32 s61, s51, s27
	s_cselect_b32 s60, s57, s26
	s_cselect_b32 s27, s45, s75
	s_cselect_b32 s26, s73, s74
	v_lshl_add_u64 v[214:215], s[58:59], 0, v[136:137]
	s_add_i32 m0, s63, 0xc000
	ds_read_b128 v[182:185], v160
	ds_read_b128 v[186:189], v160 offset:1024
	ds_read_b128 v[190:193], v160 offset:2048
	ds_read_b128 v[194:197], v160 offset:3072
	ds_read_b128 v[198:201], v160 offset:4096
	ds_read_b128 v[202:205], v160 offset:5120
	ds_read_b128 v[206:209], v160 offset:6144
	ds_read_b128 v[210:213], v160 offset:7168
	global_load_lds_dwordx4 v[214:215], off
	v_lshl_add_u64 v[214:215], s[58:59], 0, v[138:139]
	s_add_i32 m0, s63, 0xe000
	s_nop 0
	global_load_lds_dwordx4 v[214:215], off
	s_waitcnt vmcnt(8)
	s_waitcnt lgkmcnt(0)
	s_barrier
	v_mfma_f32_16x16x32_bf16 v[126:129], v[144:147], v[182:185], v[126:129]
	v_mfma_f32_16x16x32_bf16 v[122:125], v[152:155], v[182:185], v[122:125]
	v_mfma_f32_16x16x32_bf16 v[118:121], v[144:147], v[190:193], v[118:121]
	v_mfma_f32_16x16x32_bf16 v[114:117], v[152:155], v[190:193], v[114:117]
	v_mfma_f32_16x16x32_bf16 v[106:109], v[144:147], v[198:201], v[106:109]
	v_mfma_f32_16x16x32_bf16 v[98:101], v[152:155], v[198:201], v[98:101]
	v_mfma_f32_16x16x32_bf16 v[90:93], v[144:147], v[206:209], v[90:93]
	v_mfma_f32_16x16x32_bf16 v[82:85], v[152:155], v[206:209], v[82:85]
	v_mfma_f32_16x16x32_bf16 v[126:129], v[148:151], v[186:189], v[126:129]
	v_mfma_f32_16x16x32_bf16 v[122:125], v[162:165], v[186:189], v[122:125]
	v_mfma_f32_16x16x32_bf16 v[118:121], v[148:151], v[194:197], v[118:121]
	v_mfma_f32_16x16x32_bf16 v[114:117], v[162:165], v[194:197], v[114:117]
	v_mfma_f32_16x16x32_bf16 v[106:109], v[148:151], v[202:205], v[106:109]
	v_mfma_f32_16x16x32_bf16 v[98:101], v[162:165], v[202:205], v[98:101]
	v_mfma_f32_16x16x32_bf16 v[90:93], v[148:151], v[210:213], v[90:93]
	v_mfma_f32_16x16x32_bf16 v[82:85], v[162:165], v[210:213], v[82:85]
	v_mfma_f32_16x16x32_bf16 v[110:113], v[166:169], v[182:185], v[110:113]
	v_mfma_f32_16x16x32_bf16 v[102:105], v[174:177], v[182:185], v[102:105]
	v_mfma_f32_16x16x32_bf16 v[94:97], v[166:169], v[190:193], v[94:97]
	v_mfma_f32_16x16x32_bf16 v[86:89], v[174:177], v[190:193], v[86:89]
	v_mfma_f32_16x16x32_bf16 v[78:81], v[166:169], v[198:201], v[78:81]
	v_mfma_f32_16x16x32_bf16 v[74:77], v[174:177], v[198:201], v[74:77]
	v_mfma_f32_16x16x32_bf16 v[70:73], v[166:169], v[206:209], v[70:73]
	v_mfma_f32_16x16x32_bf16 v[66:69], v[174:177], v[206:209], v[66:69]
	v_mfma_f32_16x16x32_bf16 v[110:113], v[170:173], v[186:189], v[110:113]
	v_mfma_f32_16x16x32_bf16 v[102:105], v[178:181], v[186:189], v[102:105]
	v_mfma_f32_16x16x32_bf16 v[94:97], v[170:173], v[194:197], v[94:97]
	v_mfma_f32_16x16x32_bf16 v[86:89], v[178:181], v[194:197], v[86:89]
	v_mfma_f32_16x16x32_bf16 v[78:81], v[170:173], v[202:205], v[78:81]
	v_mfma_f32_16x16x32_bf16 v[74:77], v[178:181], v[202:205], v[74:77]
	v_mfma_f32_16x16x32_bf16 v[70:73], v[170:173], v[210:213], v[70:73]
	v_mfma_f32_16x16x32_bf16 v[66:69], v[178:181], v[210:213], v[66:69]
	s_barrier
	v_lshl_add_u64 v[214:215], s[26:27], 0, v[130:131]
	s_add_i32 s26, s71, s35
	s_mov_b32 m0, s26
	ds_read_b128 v[182:185], v160 offset:16384
	ds_read_b128 v[186:189], v160 offset:17408
	ds_read_b128 v[190:193], v160 offset:18432
	ds_read_b128 v[194:197], v160 offset:19456
	ds_read_b128 v[198:201], v160 offset:20480
	ds_read_b128 v[202:205], v160 offset:21504
	ds_read_b128 v[206:209], v160 offset:22528
	ds_read_b128 v[210:213], v160 offset:23552
	global_load_lds_dwordx4 v[214:215], off
	v_lshl_add_u64 v[216:217], v[214:215], 0, s[6:7]
	s_add_i32 m0, s26, 0x2000
	s_add_i32 s26, s72, s35
	global_load_lds_dwordx4 v[216:217], off
	v_lshl_add_u64 v[216:217], v[214:215], 0, s[8:9]
	s_mov_b32 m0, s26
	v_lshl_add_u64 v[220:221], s[60:61], 0, v[134:135]
	global_load_lds_dwordx4 v[216:217], off
	v_lshl_add_u64 v[216:217], v[214:215], 0, s[10:11]
	s_add_i32 m0, s26, 0x2000
	s_nop 0
	global_load_lds_dwordx4 v[216:217], off
	v_lshl_add_u64 v[216:217], s[60:61], 0, v[132:133]
	s_mov_b32 m0, s63
	s_nop 0
	global_load_lds_dwordx4 v[216:217], off
	s_mov_b32 m0, s64
	s_nop 0
	global_load_lds_dwordx4 v[220:221], off
	s_waitcnt vmcnt(8)
	s_waitcnt lgkmcnt(0)
	s_barrier
	v_mfma_f32_16x16x32_bf16 v[62:65], v[144:147], v[182:185], v[62:65]
	v_mfma_f32_16x16x32_bf16 v[58:61], v[152:155], v[182:185], v[58:61]
	v_mfma_f32_16x16x32_bf16 v[54:57], v[144:147], v[190:193], v[54:57]
	v_mfma_f32_16x16x32_bf16 v[46:49], v[152:155], v[190:193], v[46:49]
	v_mfma_f32_16x16x32_bf16 v[38:41], v[144:147], v[198:201], v[38:41]
	v_mfma_f32_16x16x32_bf16 v[30:33], v[152:155], v[198:201], v[30:33]
	v_mfma_f32_16x16x32_bf16 v[22:25], v[144:147], v[206:209], v[22:25]
	v_mfma_f32_16x16x32_bf16 v[14:17], v[152:155], v[206:209], v[14:17]
	v_mfma_f32_16x16x32_bf16 v[62:65], v[148:151], v[186:189], v[62:65]
	v_mfma_f32_16x16x32_bf16 v[58:61], v[162:165], v[186:189], v[58:61]
	v_mfma_f32_16x16x32_bf16 v[54:57], v[148:151], v[194:197], v[54:57]
	v_mfma_f32_16x16x32_bf16 v[46:49], v[162:165], v[194:197], v[46:49]
	v_mfma_f32_16x16x32_bf16 v[38:41], v[148:151], v[202:205], v[38:41]
	v_mfma_f32_16x16x32_bf16 v[30:33], v[162:165], v[202:205], v[30:33]
	v_mfma_f32_16x16x32_bf16 v[22:25], v[148:151], v[210:213], v[22:25]
	v_mfma_f32_16x16x32_bf16 v[14:17], v[162:165], v[210:213], v[14:17]
	v_mfma_f32_16x16x32_bf16 v[50:53], v[166:169], v[182:185], v[50:53]
	v_mfma_f32_16x16x32_bf16 v[42:45], v[174:177], v[182:185], v[42:45]
	v_mfma_f32_16x16x32_bf16 v[34:37], v[166:169], v[190:193], v[34:37]
	v_mfma_f32_16x16x32_bf16 v[26:29], v[174:177], v[190:193], v[26:29]
	v_mfma_f32_16x16x32_bf16 v[18:21], v[166:169], v[198:201], v[18:21]
	v_mfma_f32_16x16x32_bf16 v[10:13], v[174:177], v[198:201], v[10:13]
	v_mfma_f32_16x16x32_bf16 v[6:9], v[166:169], v[206:209], v[6:9]
	v_mfma_f32_16x16x32_bf16 v[2:5], v[174:177], v[206:209], v[2:5]
	v_mfma_f32_16x16x32_bf16 v[50:53], v[170:173], v[186:189], v[50:53]
	v_mfma_f32_16x16x32_bf16 v[42:45], v[178:181], v[186:189], v[42:45]
	v_mfma_f32_16x16x32_bf16 v[34:37], v[170:173], v[194:197], v[34:37]
	v_mfma_f32_16x16x32_bf16 v[26:29], v[178:181], v[194:197], v[26:29]
	v_mfma_f32_16x16x32_bf16 v[18:21], v[170:173], v[202:205], v[18:21]
	v_mfma_f32_16x16x32_bf16 v[10:13], v[178:181], v[202:205], v[10:13]
	v_mfma_f32_16x16x32_bf16 v[6:9], v[170:173], v[210:213], v[6:9]
	v_mfma_f32_16x16x32_bf16 v[2:5], v[178:181], v[210:213], v[2:5]
	s_barrier
	s_add_i32 s81, 0, 0x18000
	v_add_u32_e32 v161, s81, v156
	s_add_i32 s82, 0, 0x1c000
	ds_read_b128 v[144:147], v161
	ds_read_b128 v[148:151], v161 offset:1024
	ds_read_b128 v[152:155], v161 offset:2048
	ds_read_b128 v[162:165], v161 offset:3072
	v_add_u32_e32 v161, s82, v156
	ds_read_b128 v[166:169], v161
	ds_read_b128 v[170:173], v161 offset:1024
	ds_read_b128 v[174:177], v161 offset:2048
	ds_read_b128 v[178:181], v161 offset:3072
	s_add_u32 s26, s60, 0x80000
	s_addc_u32 s27, s61, 0
	s_mov_b32 m0, s65
	v_lshl_add_u64 v[222:223], s[26:27], 0, v[132:133]
	ds_read_b128 v[182:185], v160 offset:32768
	ds_read_b128 v[186:189], v160 offset:33792
	ds_read_b128 v[190:193], v160 offset:34816
	ds_read_b128 v[194:197], v160 offset:35840
	ds_read_b128 v[198:201], v160 offset:36864
	ds_read_b128 v[202:205], v160 offset:37888
	ds_read_b128 v[206:209], v160 offset:38912
	ds_read_b128 v[210:213], v160 offset:39936
	global_load_lds_dwordx4 v[222:223], off
	v_lshl_add_u64 v[222:223], s[26:27], 0, v[134:135]
	s_mov_b32 m0, s66
	s_nop 0
	global_load_lds_dwordx4 v[222:223], off
	s_waitcnt vmcnt(8)
	s_waitcnt lgkmcnt(0)
	s_barrier
	v_mfma_f32_16x16x32_bf16 v[126:129], v[144:147], v[182:185], v[126:129]
	v_mfma_f32_16x16x32_bf16 v[122:125], v[152:155], v[182:185], v[122:125]
	v_mfma_f32_16x16x32_bf16 v[118:121], v[144:147], v[190:193], v[118:121]
	v_mfma_f32_16x16x32_bf16 v[114:117], v[152:155], v[190:193], v[114:117]
	v_mfma_f32_16x16x32_bf16 v[106:109], v[144:147], v[198:201], v[106:109]
	v_mfma_f32_16x16x32_bf16 v[98:101], v[152:155], v[198:201], v[98:101]
	v_mfma_f32_16x16x32_bf16 v[90:93], v[144:147], v[206:209], v[90:93]
	v_mfma_f32_16x16x32_bf16 v[82:85], v[152:155], v[206:209], v[82:85]
	v_mfma_f32_16x16x32_bf16 v[126:129], v[148:151], v[186:189], v[126:129]
	v_mfma_f32_16x16x32_bf16 v[122:125], v[162:165], v[186:189], v[122:125]
	v_mfma_f32_16x16x32_bf16 v[118:121], v[148:151], v[194:197], v[118:121]
	v_mfma_f32_16x16x32_bf16 v[114:117], v[162:165], v[194:197], v[114:117]
	v_mfma_f32_16x16x32_bf16 v[106:109], v[148:151], v[202:205], v[106:109]
	v_mfma_f32_16x16x32_bf16 v[98:101], v[162:165], v[202:205], v[98:101]
	v_mfma_f32_16x16x32_bf16 v[90:93], v[148:151], v[210:213], v[90:93]
	v_mfma_f32_16x16x32_bf16 v[82:85], v[162:165], v[210:213], v[82:85]
	v_mfma_f32_16x16x32_bf16 v[110:113], v[166:169], v[182:185], v[110:113]
	v_mfma_f32_16x16x32_bf16 v[102:105], v[174:177], v[182:185], v[102:105]
	v_mfma_f32_16x16x32_bf16 v[94:97], v[166:169], v[190:193], v[94:97]
	v_mfma_f32_16x16x32_bf16 v[86:89], v[174:177], v[190:193], v[86:89]
	v_mfma_f32_16x16x32_bf16 v[78:81], v[166:169], v[198:201], v[78:81]
	v_mfma_f32_16x16x32_bf16 v[74:77], v[174:177], v[198:201], v[74:77]
	v_mfma_f32_16x16x32_bf16 v[70:73], v[166:169], v[206:209], v[70:73]
	v_mfma_f32_16x16x32_bf16 v[66:69], v[174:177], v[206:209], v[66:69]
	v_mfma_f32_16x16x32_bf16 v[110:113], v[170:173], v[186:189], v[110:113]
	v_mfma_f32_16x16x32_bf16 v[102:105], v[178:181], v[186:189], v[102:105]
	v_mfma_f32_16x16x32_bf16 v[94:97], v[170:173], v[194:197], v[94:97]
	v_mfma_f32_16x16x32_bf16 v[86:89], v[178:181], v[194:197], v[86:89]
	v_mfma_f32_16x16x32_bf16 v[78:81], v[170:173], v[202:205], v[78:81]
	v_mfma_f32_16x16x32_bf16 v[74:77], v[178:181], v[202:205], v[74:77]
	v_mfma_f32_16x16x32_bf16 v[70:73], v[170:173], v[210:213], v[70:73]
	v_mfma_f32_16x16x32_bf16 v[66:69], v[178:181], v[210:213], v[66:69]
	s_barrier
	s_add_i32 s26, s81, s35
	v_lshl_add_u64 v[222:223], v[214:215], 0, s[14:15]
	s_mov_b32 m0, s26
	ds_read_b128 v[182:185], v160 offset:49152
	ds_read_b128 v[186:189], v160 offset:50176
	ds_read_b128 v[190:193], v160 offset:51200
	ds_read_b128 v[194:197], v160 offset:52224
	ds_read_b128 v[198:201], v160 offset:53248
	ds_read_b128 v[202:205], v160 offset:54272
	ds_read_b128 v[206:209], v160 offset:55296
	ds_read_b128 v[210:213], v160 offset:56320
	global_load_lds_dwordx4 v[222:223], off
	v_lshl_add_u64 v[222:223], v[214:215], 0, s[16:17]
	s_add_i32 m0, s26, 0x2000
	s_add_i32 s26, s82, s35
	global_load_lds_dwordx4 v[222:223], off
	v_lshl_add_u64 v[222:223], v[214:215], 0, s[20:21]
	s_mov_b32 m0, s26
	v_lshl_add_u64 v[214:215], v[214:215], 0, s[22:23]
	global_load_lds_dwordx4 v[222:223], off
	s_add_i32 m0, s26, 0x2000
	s_nop 0
	global_load_lds_dwordx4 v[214:215], off
	v_lshl_add_u64 v[214:215], v[216:217], 0, s[18:19]
	s_mov_b32 m0, s68
	s_nop 0
	global_load_lds_dwordx4 v[214:215], off
	v_lshl_add_u64 v[214:215], v[220:221], 0, s[18:19]
	s_mov_b32 m0, s69
	s_nop 0
	global_load_lds_dwordx4 v[214:215], off
	s_waitcnt vmcnt(8)
	s_waitcnt lgkmcnt(0)
	s_barrier
	v_mfma_f32_16x16x32_bf16 v[62:65], v[144:147], v[182:185], v[62:65]
	s_add_i32 s80, s80, 2
	s_add_u32 s74, s74, 0x10000
	s_addc_u32 s75, s75, 0
	s_add_u32 s58, s58, 0x100
	s_addc_u32 s59, s59, 0
	s_cmp_gt_u32 s80, 29
	v_mfma_f32_16x16x32_bf16 v[58:61], v[152:155], v[182:185], v[58:61]
	v_mfma_f32_16x16x32_bf16 v[54:57], v[144:147], v[190:193], v[54:57]
	v_mfma_f32_16x16x32_bf16 v[46:49], v[152:155], v[190:193], v[46:49]
	v_mfma_f32_16x16x32_bf16 v[38:41], v[144:147], v[198:201], v[38:41]
	v_mfma_f32_16x16x32_bf16 v[30:33], v[152:155], v[198:201], v[30:33]
	v_mfma_f32_16x16x32_bf16 v[22:25], v[144:147], v[206:209], v[22:25]
	v_mfma_f32_16x16x32_bf16 v[14:17], v[152:155], v[206:209], v[14:17]
	v_mfma_f32_16x16x32_bf16 v[62:65], v[148:151], v[186:189], v[62:65]
	v_mfma_f32_16x16x32_bf16 v[58:61], v[162:165], v[186:189], v[58:61]
	v_mfma_f32_16x16x32_bf16 v[54:57], v[148:151], v[194:197], v[54:57]
	v_mfma_f32_16x16x32_bf16 v[46:49], v[162:165], v[194:197], v[46:49]
	v_mfma_f32_16x16x32_bf16 v[38:41], v[148:151], v[202:205], v[38:41]
	v_mfma_f32_16x16x32_bf16 v[30:33], v[162:165], v[202:205], v[30:33]
	v_mfma_f32_16x16x32_bf16 v[22:25], v[148:151], v[210:213], v[22:25]
	v_mfma_f32_16x16x32_bf16 v[14:17], v[162:165], v[210:213], v[14:17]
	v_mfma_f32_16x16x32_bf16 v[50:53], v[166:169], v[182:185], v[50:53]
	v_mfma_f32_16x16x32_bf16 v[42:45], v[174:177], v[182:185], v[42:45]
	v_mfma_f32_16x16x32_bf16 v[34:37], v[166:169], v[190:193], v[34:37]
	v_mfma_f32_16x16x32_bf16 v[26:29], v[174:177], v[190:193], v[26:29]
	v_mfma_f32_16x16x32_bf16 v[18:21], v[166:169], v[198:201], v[18:21]
	v_mfma_f32_16x16x32_bf16 v[10:13], v[174:177], v[198:201], v[10:13]
	v_mfma_f32_16x16x32_bf16 v[6:9], v[166:169], v[206:209], v[6:9]
	v_mfma_f32_16x16x32_bf16 v[2:5], v[174:177], v[206:209], v[2:5]
	v_mfma_f32_16x16x32_bf16 v[50:53], v[170:173], v[186:189], v[50:53]
	v_mfma_f32_16x16x32_bf16 v[42:45], v[178:181], v[186:189], v[42:45]
	v_mfma_f32_16x16x32_bf16 v[34:37], v[170:173], v[194:197], v[34:37]
	v_mfma_f32_16x16x32_bf16 v[26:29], v[178:181], v[194:197], v[26:29]
	v_mfma_f32_16x16x32_bf16 v[18:21], v[170:173], v[202:205], v[18:21]
	v_mfma_f32_16x16x32_bf16 v[10:13], v[178:181], v[202:205], v[10:13]
	v_mfma_f32_16x16x32_bf16 v[6:9], v[170:173], v[210:213], v[6:9]
	v_mfma_f32_16x16x32_bf16 v[2:5], v[178:181], v[210:213], v[2:5]
	s_barrier
	s_cbranch_scc0 .LBB0_1271
	s_and_b64 vcc, exec, s[24:25]
	s_cbranch_vccz .LBB0_1274
	s_barrier

.LBB0_1497:
	ds_read_b128 v[26:29], v186
	ds_read_b128 v[30:33], v186 offset:1024
	ds_read_b128 v[18:21], v186 offset:2048
	ds_read_b128 v[22:25], v186 offset:3072
	ds_read_b128 v[10:13], v187
	ds_read_b128 v[14:17], v187 offset:1024
	ds_read_b128 v[2:5], v187 offset:2048
	ds_read_b128 v[6:9], v187 offset:3072
	s_add_u32 s56, s4, 0xfffc0080
	s_addc_u32 s57, s5, -1
	s_cmp_eq_u32 s49, 12
	s_cselect_b64 vcc, -1, 0
	s_cselect_b32 s57, s2, s57
	s_cselect_b32 s56, s47, s56
	v_cndmask_b32_e32 v179, v177, v175, vcc
	v_cndmask_b32_e32 v178, v176, v174, vcc
	v_lshl_add_u64 v[180:181], s[4:5], 0, v[168:169]
	s_add_i32 m0, s62, 0xc000
	ds_read_b128 v[192:195], v188
	ds_read_b128 v[196:199], v188 offset:1024
	ds_read_b128 v[200:203], v188 offset:2048
	ds_read_b128 v[204:207], v188 offset:3072
	ds_read_b128 v[208:211], v188 offset:4096
	ds_read_b128 v[212:215], v188 offset:5120
	ds_read_b128 v[220:223], v188 offset:6144
	ds_read_b128 v[224:227], v188 offset:7168
	global_load_lds_dwordx4 v[180:181], off
	v_lshl_add_u64 v[180:181], s[4:5], 0, v[170:171]
	s_add_i32 m0, s62, 0xe000
	s_nop 0
	global_load_lds_dwordx4 v[180:181], off
	s_waitcnt vmcnt(8)
	s_waitcnt lgkmcnt(0)
	s_barrier
	v_mfma_scale_f32_16x16x128_f8f6f4 v[158:161], v[26:33], v[192:199], v[158:161], v189, v190 op_sel_hi:[0,0,0]
	v_mfma_scale_f32_16x16x128_f8f6f4 v[150:153], v[18:25], v[192:199], v[150:153], v189, v190 op_sel_hi:[0,0,0]
	v_mfma_scale_f32_16x16x128_f8f6f4 v[142:145], v[26:33], v[200:207], v[142:145], v189, v190 op_sel_hi:[0,0,0]
	v_mfma_scale_f32_16x16x128_f8f6f4 v[134:137], v[18:25], v[200:207], v[134:137], v189, v190 op_sel_hi:[0,0,0]
	v_mfma_scale_f32_16x16x128_f8f6f4 v[126:129], v[26:33], v[208:215], v[126:129], v189, v190 op_sel_hi:[0,0,0]
	v_mfma_scale_f32_16x16x128_f8f6f4 v[118:121], v[18:25], v[208:215], v[118:121], v189, v190 op_sel_hi:[0,0,0]
	v_mfma_scale_f32_16x16x128_f8f6f4 v[110:113], v[26:33], v[220:227], v[110:113], v189, v190 op_sel_hi:[0,0,0]
	v_mfma_scale_f32_16x16x128_f8f6f4 v[102:105], v[18:25], v[220:227], v[102:105], v189, v190 op_sel_hi:[0,0,0]
	v_mfma_scale_f32_16x16x128_f8f6f4 v[154:157], v[10:17], v[192:199], v[154:157], v189, v190 op_sel_hi:[0,0,0]
	v_mfma_scale_f32_16x16x128_f8f6f4 v[146:149], v[2:9], v[192:199], v[146:149], v189, v190 op_sel_hi:[0,0,0]
	v_mfma_scale_f32_16x16x128_f8f6f4 v[138:141], v[10:17], v[200:207], v[138:141], v189, v190 op_sel_hi:[0,0,0]
	v_mfma_scale_f32_16x16x128_f8f6f4 v[130:133], v[2:9], v[200:207], v[130:133], v189, v190 op_sel_hi:[0,0,0]
	v_mfma_scale_f32_16x16x128_f8f6f4 v[122:125], v[10:17], v[208:215], v[122:125], v189, v190 op_sel_hi:[0,0,0]
	v_mfma_scale_f32_16x16x128_f8f6f4 v[114:117], v[2:9], v[208:215], v[114:117], v189, v190 op_sel_hi:[0,0,0]
	v_mfma_scale_f32_16x16x128_f8f6f4 v[106:109], v[10:17], v[220:227], v[106:109], v189, v190 op_sel_hi:[0,0,0]
	v_mfma_scale_f32_16x16x128_f8f6f4 v[98:101], v[2:9], v[220:227], v[98:101], v189, v190 op_sel_hi:[0,0,0]
	s_barrier
	s_add_i32 s73, s69, s61
	v_lshl_add_u64 v[178:179], v[178:179], 0, v[162:163]
	s_mov_b32 m0, s73
	ds_read_b128 v[192:195], v188 offset:16384
	ds_read_b128 v[196:199], v188 offset:17408
	ds_read_b128 v[200:203], v188 offset:18432
	ds_read_b128 v[204:207], v188 offset:19456
	ds_read_b128 v[208:211], v188 offset:20480
	ds_read_b128 v[212:215], v188 offset:21504
	ds_read_b128 v[220:223], v188 offset:22528
	ds_read_b128 v[224:227], v188 offset:23552
	global_load_lds_dwordx4 v[178:179], off
	v_lshl_add_u64 v[180:181], v[178:179], 0, s[10:11]
	s_add_i32 m0, s73, 0x2000
	s_add_i32 s73, s70, s61
	global_load_lds_dwordx4 v[180:181], off
	v_lshl_add_u64 v[180:181], v[178:179], 0, s[12:13]
	s_mov_b32 m0, s73
	v_lshl_add_u64 v[182:183], s[56:57], 0, v[166:167]
	global_load_lds_dwordx4 v[180:181], off
	v_lshl_add_u64 v[180:181], v[178:179], 0, s[14:15]
	s_add_i32 m0, s73, 0x2000
	s_nop 0
	global_load_lds_dwordx4 v[180:181], off
	v_lshl_add_u64 v[180:181], s[56:57], 0, v[164:165]
	s_mov_b32 m0, s62
	s_nop 0
	global_load_lds_dwordx4 v[180:181], off
	s_mov_b32 m0, s53
	s_nop 0
	global_load_lds_dwordx4 v[182:183], off
	s_waitcnt vmcnt(8)
	s_waitcnt lgkmcnt(0)
	s_barrier
	v_mfma_scale_f32_16x16x128_f8f6f4 v[94:97], v[26:33], v[192:199], v[94:97], v189, v190 op_sel_hi:[0,0,0]
	v_mfma_scale_f32_16x16x128_f8f6f4 v[86:89], v[18:25], v[192:199], v[86:89], v189, v190 op_sel_hi:[0,0,0]
	v_mfma_scale_f32_16x16x128_f8f6f4 v[78:81], v[26:33], v[200:207], v[78:81], v189, v190 op_sel_hi:[0,0,0]
	v_mfma_scale_f32_16x16x128_f8f6f4 v[70:73], v[18:25], v[200:207], v[70:73], v189, v190 op_sel_hi:[0,0,0]
	v_mfma_scale_f32_16x16x128_f8f6f4 v[62:65], v[26:33], v[208:215], v[62:65], v189, v190 op_sel_hi:[0,0,0]
	v_mfma_scale_f32_16x16x128_f8f6f4 v[54:57], v[18:25], v[208:215], v[54:57], v189, v190 op_sel_hi:[0,0,0]
	v_mfma_scale_f32_16x16x128_f8f6f4 v[46:49], v[26:33], v[220:227], v[46:49], v189, v190 op_sel_hi:[0,0,0]
	v_mfma_scale_f32_16x16x128_f8f6f4 v[38:41], v[18:25], v[220:227], v[38:41], v189, v190 op_sel_hi:[0,0,0]
	v_mfma_scale_f32_16x16x128_f8f6f4 v[90:93], v[10:17], v[192:199], v[90:93], v189, v190 op_sel_hi:[0,0,0]
	v_mfma_scale_f32_16x16x128_f8f6f4 v[82:85], v[2:9], v[192:199], v[82:85], v189, v190 op_sel_hi:[0,0,0]
	v_mfma_scale_f32_16x16x128_f8f6f4 v[74:77], v[10:17], v[200:207], v[74:77], v189, v190 op_sel_hi:[0,0,0]
	v_mfma_scale_f32_16x16x128_f8f6f4 v[66:69], v[2:9], v[200:207], v[66:69], v189, v190 op_sel_hi:[0,0,0]
	v_mfma_scale_f32_16x16x128_f8f6f4 v[58:61], v[10:17], v[208:215], v[58:61], v189, v190 op_sel_hi:[0,0,0]
	v_mfma_scale_f32_16x16x128_f8f6f4 v[50:53], v[2:9], v[208:215], v[50:53], v189, v190 op_sel_hi:[0,0,0]
	v_mfma_scale_f32_16x16x128_f8f6f4 v[42:45], v[10:17], v[220:227], v[42:45], v189, v190 op_sel_hi:[0,0,0]
	v_mfma_scale_f32_16x16x128_f8f6f4 v[34:37], v[2:9], v[220:227], v[34:37], v189, v190 op_sel_hi:[0,0,0]
	s_barrier
	s_add_i32 s73, 0, 0x18000
	s_add_i32 s74, 0, 0x1c000
	v_add_u32_e32 v14, s73, v184
	v_add_u32_e32 v30, s74, v184
	ds_read_b128 v[2:5], v14
	ds_read_b128 v[6:9], v14 offset:1024
	ds_read_b128 v[10:13], v14 offset:2048
	ds_read_b128 v[14:17], v14 offset:3072
	ds_read_b128 v[18:21], v30
	ds_read_b128 v[22:25], v30 offset:1024
	ds_read_b128 v[26:29], v30 offset:2048
	ds_read_b128 v[30:33], v30 offset:3072
	s_add_u32 s56, s56, 0x40000
	s_addc_u32 s57, s57, 0
	s_mov_b32 m0, s63
	v_lshl_add_u64 v[216:217], s[56:57], 0, v[164:165]
	ds_read_b128 v[192:195], v188 offset:32768
	ds_read_b128 v[196:199], v188 offset:33792
	ds_read_b128 v[200:203], v188 offset:34816
	ds_read_b128 v[204:207], v188 offset:35840
	ds_read_b128 v[208:211], v188 offset:36864
	ds_read_b128 v[212:215], v188 offset:37888
	ds_read_b128 v[220:223], v188 offset:38912
	ds_read_b128 v[224:227], v188 offset:39936
	global_load_lds_dwordx4 v[216:217], off
	v_lshl_add_u64 v[216:217], s[56:57], 0, v[166:167]
	s_mov_b32 m0, s64
	s_nop 0
	global_load_lds_dwordx4 v[216:217], off
	s_waitcnt vmcnt(8)
	s_waitcnt lgkmcnt(0)
	s_barrier
	v_mfma_scale_f32_16x16x128_f8f6f4 v[158:161], v[2:9], v[192:199], v[158:161], v189, v190 op_sel_hi:[0,0,0]
	v_mfma_scale_f32_16x16x128_f8f6f4 v[150:153], v[10:17], v[192:199], v[150:153], v189, v190 op_sel_hi:[0,0,0]
	v_mfma_scale_f32_16x16x128_f8f6f4 v[142:145], v[2:9], v[200:207], v[142:145], v189, v190 op_sel_hi:[0,0,0]
	v_mfma_scale_f32_16x16x128_f8f6f4 v[134:137], v[10:17], v[200:207], v[134:137], v189, v190 op_sel_hi:[0,0,0]
	v_mfma_scale_f32_16x16x128_f8f6f4 v[126:129], v[2:9], v[208:215], v[126:129], v189, v190 op_sel_hi:[0,0,0]
	v_mfma_scale_f32_16x16x128_f8f6f4 v[118:121], v[10:17], v[208:215], v[118:121], v189, v190 op_sel_hi:[0,0,0]
	v_mfma_scale_f32_16x16x128_f8f6f4 v[110:113], v[2:9], v[220:227], v[110:113], v189, v190 op_sel_hi:[0,0,0]
	v_mfma_scale_f32_16x16x128_f8f6f4 v[102:105], v[10:17], v[220:227], v[102:105], v189, v190 op_sel_hi:[0,0,0]
	v_mfma_scale_f32_16x16x128_f8f6f4 v[154:157], v[18:25], v[192:199], v[154:157], v189, v190 op_sel_hi:[0,0,0]
	v_mfma_scale_f32_16x16x128_f8f6f4 v[146:149], v[26:33], v[192:199], v[146:149], v189, v190 op_sel_hi:[0,0,0]
	v_mfma_scale_f32_16x16x128_f8f6f4 v[138:141], v[18:25], v[200:207], v[138:141], v189, v190 op_sel_hi:[0,0,0]
	v_mfma_scale_f32_16x16x128_f8f6f4 v[130:133], v[26:33], v[200:207], v[130:133], v189, v190 op_sel_hi:[0,0,0]
	v_mfma_scale_f32_16x16x128_f8f6f4 v[122:125], v[18:25], v[208:215], v[122:125], v189, v190 op_sel_hi:[0,0,0]
	v_mfma_scale_f32_16x16x128_f8f6f4 v[114:117], v[26:33], v[208:215], v[114:117], v189, v190 op_sel_hi:[0,0,0]
	v_mfma_scale_f32_16x16x128_f8f6f4 v[106:109], v[18:25], v[220:227], v[106:109], v189, v190 op_sel_hi:[0,0,0]
	v_mfma_scale_f32_16x16x128_f8f6f4 v[98:101], v[26:33], v[220:227], v[98:101], v189, v190 op_sel_hi:[0,0,0]
	s_barrier
	s_add_i32 s56, s73, s61
	v_lshl_add_u64 v[216:217], v[178:179], 0, s[20:21]
	s_mov_b32 m0, s56
	ds_read_b128 v[192:195], v188 offset:49152
	ds_read_b128 v[196:199], v188 offset:50176
	ds_read_b128 v[200:203], v188 offset:51200
	ds_read_b128 v[204:207], v188 offset:52224
	ds_read_b128 v[208:211], v188 offset:53248
	ds_read_b128 v[212:215], v188 offset:54272
	ds_read_b128 v[220:223], v188 offset:55296
	ds_read_b128 v[224:227], v188 offset:56320
	global_load_lds_dwordx4 v[216:217], off
	v_lshl_add_u64 v[216:217], v[178:179], 0, s[22:23]
	s_add_i32 m0, s56, 0x2000
	s_add_i32 s56, s74, s61
	global_load_lds_dwordx4 v[216:217], off
	v_lshl_add_u64 v[216:217], v[178:179], 0, s[26:27]
	s_mov_b32 m0, s56
	v_lshl_add_u64 v[178:179], v[178:179], 0, s[36:37]
	global_load_lds_dwordx4 v[216:217], off
	s_add_i32 m0, s56, 0x2000
	s_nop 0
	global_load_lds_dwordx4 v[178:179], off
	v_lshl_add_u64 v[178:179], v[180:181], 0, s[24:25]
	s_mov_b32 m0, s66
	s_nop 0
	global_load_lds_dwordx4 v[178:179], off
	v_lshl_add_u64 v[178:179], v[182:183], 0, s[24:25]
	s_mov_b32 m0, s67
	s_nop 0
	global_load_lds_dwordx4 v[178:179], off
	s_waitcnt vmcnt(8)
	s_waitcnt lgkmcnt(0)
	s_barrier
	v_mfma_scale_f32_16x16x128_f8f6f4 v[94:97], v[2:9], v[192:199], v[94:97], v189, v190 op_sel_hi:[0,0,0]
	s_add_i32 s49, s49, 2
	s_add_u32 s4, s4, 0x100
	s_addc_u32 s5, s5, 0
	s_cmp_gt_u32 s49, 13
	v_lshl_add_u64 v[176:177], v[176:177], 0, s[40:41]
	v_mfma_scale_f32_16x16x128_f8f6f4 v[86:89], v[10:17], v[192:199], v[86:89], v189, v190 op_sel_hi:[0,0,0]
	v_mfma_scale_f32_16x16x128_f8f6f4 v[78:81], v[2:9], v[200:207], v[78:81], v189, v190 op_sel_hi:[0,0,0]
	v_mfma_scale_f32_16x16x128_f8f6f4 v[70:73], v[10:17], v[200:207], v[70:73], v189, v190 op_sel_hi:[0,0,0]
	v_mfma_scale_f32_16x16x128_f8f6f4 v[62:65], v[2:9], v[208:215], v[62:65], v189, v190 op_sel_hi:[0,0,0]
	v_mfma_scale_f32_16x16x128_f8f6f4 v[54:57], v[10:17], v[208:215], v[54:57], v189, v190 op_sel_hi:[0,0,0]
	v_mfma_scale_f32_16x16x128_f8f6f4 v[46:49], v[2:9], v[220:227], v[46:49], v189, v190 op_sel_hi:[0,0,0]
	v_mfma_scale_f32_16x16x128_f8f6f4 v[38:41], v[10:17], v[220:227], v[38:41], v189, v190 op_sel_hi:[0,0,0]
	v_mfma_scale_f32_16x16x128_f8f6f4 v[90:93], v[18:25], v[192:199], v[90:93], v189, v190 op_sel_hi:[0,0,0]
	v_mfma_scale_f32_16x16x128_f8f6f4 v[82:85], v[26:33], v[192:199], v[82:85], v189, v190 op_sel_hi:[0,0,0]
	v_mfma_scale_f32_16x16x128_f8f6f4 v[74:77], v[18:25], v[200:207], v[74:77], v189, v190 op_sel_hi:[0,0,0]
	v_mfma_scale_f32_16x16x128_f8f6f4 v[66:69], v[26:33], v[200:207], v[66:69], v189, v190 op_sel_hi:[0,0,0]
	v_mfma_scale_f32_16x16x128_f8f6f4 v[58:61], v[18:25], v[208:215], v[58:61], v189, v190 op_sel_hi:[0,0,0]
	v_mfma_scale_f32_16x16x128_f8f6f4 v[50:53], v[26:33], v[208:215], v[50:53], v189, v190 op_sel_hi:[0,0,0]
	v_mfma_scale_f32_16x16x128_f8f6f4 v[42:45], v[18:25], v[220:227], v[42:45], v189, v190 op_sel_hi:[0,0,0]
	v_mfma_scale_f32_16x16x128_f8f6f4 v[34:37], v[26:33], v[220:227], v[34:37], v189, v190 op_sel_hi:[0,0,0]
	s_barrier
	s_cbranch_scc0 .LBB0_1497
	s_and_b64 vcc, exec, s[38:39]
	s_cbranch_vccz .LBB0_1500
	s_barrier

.LBB0_1568:
	ds_read_b128 v[26:29], v186
	ds_read_b128 v[30:33], v186 offset:1024
	ds_read_b128 v[18:21], v186 offset:2048
	ds_read_b128 v[22:25], v186 offset:3072
	ds_read_b128 v[10:13], v187
	ds_read_b128 v[14:17], v187 offset:1024
	ds_read_b128 v[2:5], v187 offset:2048
	ds_read_b128 v[6:9], v187 offset:3072
	s_add_u32 s58, s56, 0xfff50080
	s_addc_u32 s59, s57, -1
	s_cmp_eq_u32 s53, 40
	s_cselect_b64 vcc, -1, 0
	s_cselect_b32 s59, s5, s59
	s_cselect_b32 s58, s4, s58
	v_cndmask_b32_e32 v179, v177, v175, vcc
	v_cndmask_b32_e32 v178, v176, v174, vcc
	v_lshl_add_u64 v[180:181], s[56:57], 0, v[170:171]
	s_add_i32 m0, s61, 0xc000
	ds_read_b128 v[192:195], v188
	ds_read_b128 v[196:199], v188 offset:1024
	ds_read_b128 v[200:203], v188 offset:2048
	ds_read_b128 v[204:207], v188 offset:3072
	ds_read_b128 v[208:211], v188 offset:4096
	ds_read_b128 v[212:215], v188 offset:5120
	ds_read_b128 v[220:223], v188 offset:6144
	ds_read_b128 v[224:227], v188 offset:7168
	global_load_lds_dwordx4 v[180:181], off
	v_lshl_add_u64 v[180:181], s[56:57], 0, v[172:173]
	s_add_i32 m0, s61, 0xe000
	s_nop 0
	global_load_lds_dwordx4 v[180:181], off
	s_waitcnt vmcnt(8)
	s_waitcnt lgkmcnt(0)
	s_barrier
	v_mfma_scale_f32_16x16x128_f8f6f4 v[158:161], v[26:33], v[192:199], v[158:161], v189, v190 op_sel_hi:[0,0,0]
	v_mfma_scale_f32_16x16x128_f8f6f4 v[154:157], v[18:25], v[192:199], v[154:157], v189, v190 op_sel_hi:[0,0,0]
	v_mfma_scale_f32_16x16x128_f8f6f4 v[150:153], v[26:33], v[200:207], v[150:153], v189, v190 op_sel_hi:[0,0,0]
	v_mfma_scale_f32_16x16x128_f8f6f4 v[142:145], v[18:25], v[200:207], v[142:145], v189, v190 op_sel_hi:[0,0,0]
	v_mfma_scale_f32_16x16x128_f8f6f4 v[134:137], v[26:33], v[208:215], v[134:137], v189, v190 op_sel_hi:[0,0,0]
	v_mfma_scale_f32_16x16x128_f8f6f4 v[126:129], v[18:25], v[208:215], v[126:129], v189, v190 op_sel_hi:[0,0,0]
	v_mfma_scale_f32_16x16x128_f8f6f4 v[118:121], v[26:33], v[220:227], v[118:121], v189, v190 op_sel_hi:[0,0,0]
	v_mfma_scale_f32_16x16x128_f8f6f4 v[110:113], v[18:25], v[220:227], v[110:113], v189, v190 op_sel_hi:[0,0,0]
	v_mfma_scale_f32_16x16x128_f8f6f4 v[146:149], v[10:17], v[192:199], v[146:149], v189, v190 op_sel_hi:[0,0,0]
	v_mfma_scale_f32_16x16x128_f8f6f4 v[138:141], v[2:9], v[192:199], v[138:141], v189, v190 op_sel_hi:[0,0,0]
	v_mfma_scale_f32_16x16x128_f8f6f4 v[130:133], v[10:17], v[200:207], v[130:133], v189, v190 op_sel_hi:[0,0,0]
	v_mfma_scale_f32_16x16x128_f8f6f4 v[122:125], v[2:9], v[200:207], v[122:125], v189, v190 op_sel_hi:[0,0,0]
	v_mfma_scale_f32_16x16x128_f8f6f4 v[114:117], v[10:17], v[208:215], v[114:117], v189, v190 op_sel_hi:[0,0,0]
	v_mfma_scale_f32_16x16x128_f8f6f4 v[106:109], v[2:9], v[208:215], v[106:109], v189, v190 op_sel_hi:[0,0,0]
	v_mfma_scale_f32_16x16x128_f8f6f4 v[102:105], v[10:17], v[220:227], v[102:105], v189, v190 op_sel_hi:[0,0,0]
	v_mfma_scale_f32_16x16x128_f8f6f4 v[98:101], v[2:9], v[220:227], v[98:101], v189, v190 op_sel_hi:[0,0,0]
	s_barrier
	s_add_i32 s80, s69, s33
	v_lshl_add_u64 v[178:179], v[178:179], 0, v[164:165]
	s_mov_b32 m0, s80
	ds_read_b128 v[192:195], v188 offset:16384
	ds_read_b128 v[196:199], v188 offset:17408
	ds_read_b128 v[200:203], v188 offset:18432
	ds_read_b128 v[204:207], v188 offset:19456
	ds_read_b128 v[208:211], v188 offset:20480
	ds_read_b128 v[212:215], v188 offset:21504
	ds_read_b128 v[220:223], v188 offset:22528
	ds_read_b128 v[224:227], v188 offset:23552
	global_load_lds_dwordx4 v[178:179], off
	v_lshl_add_u64 v[180:181], v[178:179], 0, s[10:11]
	s_add_i32 m0, s80, 0x2000
	s_add_i32 s80, s70, s33
	global_load_lds_dwordx4 v[180:181], off
	v_lshl_add_u64 v[180:181], v[178:179], 0, s[12:13]
	s_mov_b32 m0, s80
	v_lshl_add_u64 v[182:183], s[58:59], 0, v[168:169]
	global_load_lds_dwordx4 v[180:181], off
	v_lshl_add_u64 v[180:181], v[178:179], 0, s[14:15]
	s_add_i32 m0, s80, 0x2000
	s_nop 0
	global_load_lds_dwordx4 v[180:181], off
	v_lshl_add_u64 v[180:181], s[58:59], 0, v[166:167]
	s_mov_b32 m0, s61
	s_nop 0
	global_load_lds_dwordx4 v[180:181], off
	s_mov_b32 m0, s62
	s_nop 0
	global_load_lds_dwordx4 v[182:183], off
	s_waitcnt vmcnt(8)
	s_waitcnt lgkmcnt(0)
	s_barrier
	v_mfma_scale_f32_16x16x128_f8f6f4 v[94:97], v[26:33], v[192:199], v[94:97], v189, v190 op_sel_hi:[0,0,0]
	v_mfma_scale_f32_16x16x128_f8f6f4 v[90:93], v[18:25], v[192:199], v[90:93], v189, v190 op_sel_hi:[0,0,0]
	v_mfma_scale_f32_16x16x128_f8f6f4 v[86:89], v[26:33], v[200:207], v[86:89], v189, v190 op_sel_hi:[0,0,0]
	v_mfma_scale_f32_16x16x128_f8f6f4 v[78:81], v[18:25], v[200:207], v[78:81], v189, v190 op_sel_hi:[0,0,0]
	v_mfma_scale_f32_16x16x128_f8f6f4 v[70:73], v[26:33], v[208:215], v[70:73], v189, v190 op_sel_hi:[0,0,0]
	v_mfma_scale_f32_16x16x128_f8f6f4 v[62:65], v[18:25], v[208:215], v[62:65], v189, v190 op_sel_hi:[0,0,0]
	v_mfma_scale_f32_16x16x128_f8f6f4 v[54:57], v[26:33], v[220:227], v[54:57], v189, v190 op_sel_hi:[0,0,0]
	v_mfma_scale_f32_16x16x128_f8f6f4 v[46:49], v[18:25], v[220:227], v[46:49], v189, v190 op_sel_hi:[0,0,0]
	v_mfma_scale_f32_16x16x128_f8f6f4 v[82:85], v[10:17], v[192:199], v[82:85], v189, v190 op_sel_hi:[0,0,0]
	v_mfma_scale_f32_16x16x128_f8f6f4 v[74:77], v[2:9], v[192:199], v[74:77], v189, v190 op_sel_hi:[0,0,0]
	v_mfma_scale_f32_16x16x128_f8f6f4 v[66:69], v[10:17], v[200:207], v[66:69], v189, v190 op_sel_hi:[0,0,0]
	v_mfma_scale_f32_16x16x128_f8f6f4 v[58:61], v[2:9], v[200:207], v[58:61], v189, v190 op_sel_hi:[0,0,0]
	v_mfma_scale_f32_16x16x128_f8f6f4 v[50:53], v[10:17], v[208:215], v[50:53], v189, v190 op_sel_hi:[0,0,0]
	v_mfma_scale_f32_16x16x128_f8f6f4 v[42:45], v[2:9], v[208:215], v[42:45], v189, v190 op_sel_hi:[0,0,0]
	v_mfma_scale_f32_16x16x128_f8f6f4 v[38:41], v[10:17], v[220:227], v[38:41], v189, v190 op_sel_hi:[0,0,0]
	v_mfma_scale_f32_16x16x128_f8f6f4 v[34:37], v[2:9], v[220:227], v[34:37], v189, v190 op_sel_hi:[0,0,0]
	s_barrier
	s_add_i32 s80, 0, 0x18000
	s_add_i32 s81, 0, 0x1c000
	v_add_u32_e32 v14, s80, v184
	v_add_u32_e32 v30, s81, v184
	ds_read_b128 v[2:5], v14
	ds_read_b128 v[6:9], v14 offset:1024
	ds_read_b128 v[10:13], v14 offset:2048
	ds_read_b128 v[14:17], v14 offset:3072
	ds_read_b128 v[18:21], v30
	ds_read_b128 v[22:25], v30 offset:1024
	ds_read_b128 v[26:29], v30 offset:2048
	ds_read_b128 v[30:33], v30 offset:3072
	s_add_u32 s58, s58, 0xb0000
	s_addc_u32 s59, s59, 0
	s_mov_b32 m0, s63
	v_lshl_add_u64 v[216:217], s[58:59], 0, v[166:167]
	ds_read_b128 v[192:195], v188 offset:32768
	ds_read_b128 v[196:199], v188 offset:33792
	ds_read_b128 v[200:203], v188 offset:34816
	ds_read_b128 v[204:207], v188 offset:35840
	ds_read_b128 v[208:211], v188 offset:36864
	ds_read_b128 v[212:215], v188 offset:37888
	ds_read_b128 v[220:223], v188 offset:38912
	ds_read_b128 v[224:227], v188 offset:39936
	global_load_lds_dwordx4 v[216:217], off
	v_lshl_add_u64 v[216:217], s[58:59], 0, v[168:169]
	s_mov_b32 m0, s64
	s_nop 0
	global_load_lds_dwordx4 v[216:217], off
	s_waitcnt vmcnt(8)
	s_waitcnt lgkmcnt(0)
	s_barrier
	v_mfma_scale_f32_16x16x128_f8f6f4 v[158:161], v[2:9], v[192:199], v[158:161], v189, v190 op_sel_hi:[0,0,0]
	v_mfma_scale_f32_16x16x128_f8f6f4 v[154:157], v[10:17], v[192:199], v[154:157], v189, v190 op_sel_hi:[0,0,0]
	v_mfma_scale_f32_16x16x128_f8f6f4 v[150:153], v[2:9], v[200:207], v[150:153], v189, v190 op_sel_hi:[0,0,0]
	v_mfma_scale_f32_16x16x128_f8f6f4 v[142:145], v[10:17], v[200:207], v[142:145], v189, v190 op_sel_hi:[0,0,0]
	v_mfma_scale_f32_16x16x128_f8f6f4 v[134:137], v[2:9], v[208:215], v[134:137], v189, v190 op_sel_hi:[0,0,0]
	v_mfma_scale_f32_16x16x128_f8f6f4 v[126:129], v[10:17], v[208:215], v[126:129], v189, v190 op_sel_hi:[0,0,0]
	v_mfma_scale_f32_16x16x128_f8f6f4 v[118:121], v[2:9], v[220:227], v[118:121], v189, v190 op_sel_hi:[0,0,0]
	v_mfma_scale_f32_16x16x128_f8f6f4 v[110:113], v[10:17], v[220:227], v[110:113], v189, v190 op_sel_hi:[0,0,0]
	v_mfma_scale_f32_16x16x128_f8f6f4 v[146:149], v[18:25], v[192:199], v[146:149], v189, v190 op_sel_hi:[0,0,0]
	v_mfma_scale_f32_16x16x128_f8f6f4 v[138:141], v[26:33], v[192:199], v[138:141], v189, v190 op_sel_hi:[0,0,0]
	v_mfma_scale_f32_16x16x128_f8f6f4 v[130:133], v[18:25], v[200:207], v[130:133], v189, v190 op_sel_hi:[0,0,0]
	v_mfma_scale_f32_16x16x128_f8f6f4 v[122:125], v[26:33], v[200:207], v[122:125], v189, v190 op_sel_hi:[0,0,0]
	v_mfma_scale_f32_16x16x128_f8f6f4 v[114:117], v[18:25], v[208:215], v[114:117], v189, v190 op_sel_hi:[0,0,0]
	v_mfma_scale_f32_16x16x128_f8f6f4 v[106:109], v[26:33], v[208:215], v[106:109], v189, v190 op_sel_hi:[0,0,0]
	v_mfma_scale_f32_16x16x128_f8f6f4 v[102:105], v[18:25], v[220:227], v[102:105], v189, v190 op_sel_hi:[0,0,0]
	v_mfma_scale_f32_16x16x128_f8f6f4 v[98:101], v[26:33], v[220:227], v[98:101], v189, v190 op_sel_hi:[0,0,0]
	s_barrier
	s_add_i32 s58, s80, s33
	v_lshl_add_u64 v[216:217], v[178:179], 0, s[24:25]
	s_mov_b32 m0, s58
	ds_read_b128 v[192:195], v188 offset:49152
	ds_read_b128 v[196:199], v188 offset:50176
	ds_read_b128 v[200:203], v188 offset:51200
	ds_read_b128 v[204:207], v188 offset:52224
	ds_read_b128 v[208:211], v188 offset:53248
	ds_read_b128 v[212:215], v188 offset:54272
	ds_read_b128 v[220:223], v188 offset:55296
	ds_read_b128 v[224:227], v188 offset:56320
	global_load_lds_dwordx4 v[216:217], off
	v_lshl_add_u64 v[216:217], v[178:179], 0, s[26:27]
	s_add_i32 m0, s58, 0x2000
	s_add_i32 s58, s81, s33
	global_load_lds_dwordx4 v[216:217], off
	v_lshl_add_u64 v[216:217], v[178:179], 0, s[38:39]
	s_mov_b32 m0, s58
	v_lshl_add_u64 v[178:179], v[178:179], 0, s[40:41]
	global_load_lds_dwordx4 v[216:217], off
	s_add_i32 m0, s58, 0x2000
	s_nop 0
	global_load_lds_dwordx4 v[178:179], off
	v_lshl_add_u64 v[178:179], v[180:181], 0, s[36:37]
	s_mov_b32 m0, s66
	s_nop 0
	global_load_lds_dwordx4 v[178:179], off
	v_lshl_add_u64 v[178:179], v[182:183], 0, s[36:37]
	s_mov_b32 m0, s67
	s_nop 0
	global_load_lds_dwordx4 v[178:179], off
	s_waitcnt vmcnt(8)
	s_waitcnt lgkmcnt(0)
	s_barrier
	v_mfma_scale_f32_16x16x128_f8f6f4 v[94:97], v[2:9], v[192:199], v[94:97], v189, v190 op_sel_hi:[0,0,0]
	s_add_i32 s53, s53, 2
	s_add_u32 s56, s56, 0x100
	s_addc_u32 s57, s57, 0
	s_cmp_gt_u32 s53, 41
	v_lshl_add_u64 v[176:177], v[176:177], 0, s[44:45]
	v_mfma_scale_f32_16x16x128_f8f6f4 v[90:93], v[10:17], v[192:199], v[90:93], v189, v190 op_sel_hi:[0,0,0]
	v_mfma_scale_f32_16x16x128_f8f6f4 v[86:89], v[2:9], v[200:207], v[86:89], v189, v190 op_sel_hi:[0,0,0]
	v_mfma_scale_f32_16x16x128_f8f6f4 v[78:81], v[10:17], v[200:207], v[78:81], v189, v190 op_sel_hi:[0,0,0]
	v_mfma_scale_f32_16x16x128_f8f6f4 v[70:73], v[2:9], v[208:215], v[70:73], v189, v190 op_sel_hi:[0,0,0]
	v_mfma_scale_f32_16x16x128_f8f6f4 v[62:65], v[10:17], v[208:215], v[62:65], v189, v190 op_sel_hi:[0,0,0]
	v_mfma_scale_f32_16x16x128_f8f6f4 v[54:57], v[2:9], v[220:227], v[54:57], v189, v190 op_sel_hi:[0,0,0]
	v_mfma_scale_f32_16x16x128_f8f6f4 v[46:49], v[10:17], v[220:227], v[46:49], v189, v190 op_sel_hi:[0,0,0]
	v_mfma_scale_f32_16x16x128_f8f6f4 v[82:85], v[18:25], v[192:199], v[82:85], v189, v190 op_sel_hi:[0,0,0]
	v_mfma_scale_f32_16x16x128_f8f6f4 v[74:77], v[26:33], v[192:199], v[74:77], v189, v190 op_sel_hi:[0,0,0]
	v_mfma_scale_f32_16x16x128_f8f6f4 v[66:69], v[18:25], v[200:207], v[66:69], v189, v190 op_sel_hi:[0,0,0]
	v_mfma_scale_f32_16x16x128_f8f6f4 v[58:61], v[26:33], v[200:207], v[58:61], v189, v190 op_sel_hi:[0,0,0]
	v_mfma_scale_f32_16x16x128_f8f6f4 v[50:53], v[18:25], v[208:215], v[50:53], v189, v190 op_sel_hi:[0,0,0]
	v_mfma_scale_f32_16x16x128_f8f6f4 v[42:45], v[26:33], v[208:215], v[42:45], v189, v190 op_sel_hi:[0,0,0]
	v_mfma_scale_f32_16x16x128_f8f6f4 v[38:41], v[18:25], v[220:227], v[38:41], v189, v190 op_sel_hi:[0,0,0]
	v_mfma_scale_f32_16x16x128_f8f6f4 v[34:37], v[26:33], v[220:227], v[34:37], v189, v190 op_sel_hi:[0,0,0]
	s_barrier
	s_cbranch_scc0 .LBB0_1568
	s_and_b64 vcc, exec, s[42:43]
	s_cbranch_vccz .LBB0_1571
	s_barrier
